# v35 + priority inversion in the six GEMM K-loops: memory phase (ds_reads + LDS-DMA issue) at prio 1, MFMA block at prio 0
# speedup vs baseline: 1.0144x; 1.0144x over previous
; #define PG8_STAGE(bufoff, RS, soff, voff) do { _Pragma("unroll") for (int _i = 0; _i < 2; ++_i) \
;         __builtin_amdgcn_raw_ptr_buffer_load_lds(RS, (PG8_LAS void*)(lds + (bufoff) + sgpr_opaque(ldsw) + _i * 8192), 16, (int)(voff)[_i], (int)(soff), 0, 0); } while (0)
; #define PG8_LDA(dst, b, h) do { _Pragma("unroll") for (int m = 0; m < 4; ++m) _Pragma("unroll") for (int k = 0; k < 2; ++k) dst[m][k] = *(const PG8_LAS f16x8*)(lds + PG8_SA(b, h) + aoff + m * 2048 + k * 1024); } while (0)
; #define PG8_LDB(dst, b, h) do { _Pragma("unroll") for (int n = 0; n < 2; ++n) _Pragma("unroll") for (int k = 0; k < 2; ++k) dst[n][k] = *(const PG8_LAS f16x8*)(lds + PG8_SB(b, h) + boff + n * 2048 + k * 1024); } while (0)
; #define PG8_WAIT_L(n) asm volatile("s_waitcnt lgkmcnt(" #n ")" ::: "memory")
; #define PG8_BAR __builtin_amdgcn_s_barrier()
; #define PG8_SCHED __builtin_amdgcn_sched_barrier(0)
; template <class Epi, class Sched, bool ALIGN_EPI = false, bool SP2 = false, bool I8 = false, bool ATILED = false>
; __device__ __forceinline__ void gemm_phase(PG8_LAS unsigned char* lds, const Gemm g, const Sched& S, const Epi& E, const int wid) {
;     ...
;             PG8_LDB(B0, 0, 0); PG8_LDB(B1, 0, 1); PG8_SCHED; PG8_LDA(At, 0, 0); PG8_STAGE(PG8_SA(1, 1), rsA, a1 + hstepA, voffA);
;             PG8_WAIT_VG; PG8_WAIT_L(0); PG8_BAR; PG8_MMA(0, 0, At, B0); PG8_MMA(0, 1, At, B1); PG8_BAR; PG8_SCHED;
;             PG8_LDA(At, 0, 1); PG8_STAGE(PG8_SB(0, 0), rsB, b2, voffB); PG8_STAGE(PG8_SB(0, 1), rsB, b2 + hstep, voffB); PG8_STAGE(PG8_SA(0, 0), rsA, a2, voffA);
;             PG8_WAIT_VG; PG8_WAIT_L(0); PG8_BAR; PG8_MMA(1, 0, At, B0); PG8_MMA(1, 1, At, B1); PG8_BAR; PG8_SCHED;
;             PG8_LDB(B0, 1, 0); PG8_LDB(B1, 1, 1); PG8_SCHED; PG8_LDA(At, 1, 0); PG8_STAGE(PG8_SA(0, 1), rsA, a2 + hstepA, voffA);
;             PG8_WAIT_VG; PG8_WAIT_L(0); PG8_BAR; PG8_MMA(0, 0, At, B0); PG8_MMA(0, 1, At, B1); PG8_BAR; PG8_SCHED;
;             PG8_LDA(At, 1, 1); PG8_STAGE(PG8_SB(1, 0), rsB, b3, voffB); PG8_STAGE(PG8_SB(1, 1), rsB, b3 + hstep, voffB); PG8_STAGE(PG8_SA(1, 0), rsA, a3, voffA);
;             PG8_WAIT_VG; PG8_WAIT_L(0); PG8_BAR; PG8_MMA(1, 0, At, B0); PG8_MMA(1, 1, At, B1); PG8_BAR; PG8_SCHED;
.Lgr0:
	s_waitcnt vmcnt(24)
	s_waitcnt lgkmcnt(0)
	s_barrier
	s_setprio 0
	s_waitcnt lgkmcnt(7)
	v_mfma_i32_16x16x64_i8 v[126:129], v[130:133], v[162:165], v[126:129]
	v_mfma_i32_16x16x64_i8 v[122:125], v[138:141], v[162:165], v[122:125]
	s_waitcnt lgkmcnt(5)
	v_mfma_i32_16x16x64_i8 v[110:113], v[130:133], v[182:185], v[110:113]
	v_mfma_i32_16x16x64_i8 v[106:109], v[138:141], v[182:185], v[106:109]
	s_waitcnt lgkmcnt(3)
	v_mfma_i32_16x16x64_i8 v[94:97], v[130:133], v[190:193], v[94:97]
	v_mfma_i32_16x16x64_i8 v[90:93], v[138:141], v[190:193], v[90:93]
	s_waitcnt lgkmcnt(1)
	v_mfma_i32_16x16x64_i8 v[78:81], v[130:133], v[208:211], v[78:81]
	v_mfma_i32_16x16x64_i8 v[74:77], v[138:141], v[208:211], v[74:77]
	v_mfma_i32_16x16x64_i8 v[126:129], v[134:137], v[166:169], v[126:129]
	v_mfma_i32_16x16x64_i8 v[122:125], v[142:145], v[166:169], v[122:125]
	v_mfma_i32_16x16x64_i8 v[110:113], v[134:137], v[186:189], v[110:113]
	v_mfma_i32_16x16x64_i8 v[106:109], v[142:145], v[186:189], v[106:109]
	v_mfma_i32_16x16x64_i8 v[94:97], v[134:137], v[194:197], v[94:97]
	v_mfma_i32_16x16x64_i8 v[90:93], v[142:145], v[194:197], v[90:93]
	s_waitcnt lgkmcnt(0)
	v_mfma_i32_16x16x64_i8 v[78:81], v[134:137], v[212:215], v[78:81]
	v_mfma_i32_16x16x64_i8 v[74:77], v[142:145], v[212:215], v[74:77]
	s_setprio 1
	s_setprio 0
	v_mfma_i32_16x16x64_i8 v[118:121], v[146:149], v[162:165], v[118:121]
	v_mfma_i32_16x16x64_i8 v[114:117], v[154:157], v[162:165], v[114:117]
	v_mfma_i32_16x16x64_i8 v[102:105], v[146:149], v[182:185], v[102:105]
	v_mfma_i32_16x16x64_i8 v[98:101], v[154:157], v[182:185], v[98:101]
	v_mfma_i32_16x16x64_i8 v[86:89], v[146:149], v[190:193], v[86:89]
	v_mfma_i32_16x16x64_i8 v[82:85], v[154:157], v[190:193], v[82:85]
	v_mfma_i32_16x16x64_i8 v[70:73], v[146:149], v[208:211], v[70:73]
	v_mfma_i32_16x16x64_i8 v[66:69], v[154:157], v[208:211], v[66:69]
	v_mfma_i32_16x16x64_i8 v[118:121], v[150:153], v[166:169], v[118:121]
	v_mfma_i32_16x16x64_i8 v[114:117], v[158:161], v[166:169], v[114:117]
	v_mfma_i32_16x16x64_i8 v[102:105], v[150:153], v[186:189], v[102:105]
	v_mfma_i32_16x16x64_i8 v[98:101], v[158:161], v[186:189], v[98:101]
	v_mfma_i32_16x16x64_i8 v[86:89], v[150:153], v[194:197], v[86:89]
	v_mfma_i32_16x16x64_i8 v[82:85], v[158:161], v[194:197], v[82:85]
	v_mfma_i32_16x16x64_i8 v[70:73], v[150:153], v[212:215], v[70:73]
	v_mfma_i32_16x16x64_i8 v[66:69], v[158:161], v[212:215], v[66:69]
	s_setprio 1
	s_barrier
	s_mov_b32 s55, s85
	ds_read_b128 v[162:165], v177 offset:16384
	ds_read_b128 v[166:169], v177 offset:17408
	ds_read_b128 v[182:185], v177 offset:18432
	ds_read_b128 v[186:189], v177 offset:19456
	ds_read_b128 v[190:193], v177 offset:20480
	ds_read_b128 v[194:197], v177 offset:21504
	ds_read_b128 v[208:211], v177 offset:22528
	ds_read_b128 v[212:215], v177 offset:23552
	s_add_i32 m0, s55, 0x10000
	s_mov_b32 s55, s85
	buffer_load_dwordx4 v172, s[64:67], s51 offen lds
	s_add_i32 m0, s55, 0x12000
	s_mov_b32 s58, s85
	buffer_load_dwordx4 v174, s[64:67], s51 offen lds
	s_add_i32 s55, s51, 0x4000
	s_add_i32 m0, s58, 0x14000
	s_mov_b32 s58, s85
	buffer_load_dwordx4 v172, s[64:67], s55 offen lds
	s_add_i32 m0, s58, 0x16000
	s_nop 0
	buffer_load_dwordx4 v174, s[64:67], s55 offen lds
	s_mov_b32 s55, s85
	s_mov_b32 m0, s55
	s_mov_b32 s55, s85
	buffer_load_dwordx4 v0, s[88:91], s54 offen lds
	s_add_i32 m0, s55, 0x2000
	s_nop 0
	buffer_load_dwordx4 v173, s[88:91], s54 offen lds
	s_cmp_lg_u32 s53, 0
	s_cbranch_scc1 .Lgr1
	s_waitcnt vmcnt(8)
.Lgr1:
	s_waitcnt vmcnt(24)
	s_waitcnt lgkmcnt(0)
	s_barrier
	s_setprio 0
	s_waitcnt lgkmcnt(7)
	v_mfma_i32_16x16x64_i8 v[62:65], v[130:133], v[162:165], v[62:65]
	v_mfma_i32_16x16x64_i8 v[58:61], v[138:141], v[162:165], v[58:61]
	s_waitcnt lgkmcnt(5)
	v_mfma_i32_16x16x64_i8 v[46:49], v[130:133], v[182:185], v[46:49]
	v_mfma_i32_16x16x64_i8 v[42:45], v[138:141], v[182:185], v[42:45]
	s_waitcnt lgkmcnt(3)
	v_mfma_i32_16x16x64_i8 v[30:33], v[130:133], v[190:193], v[30:33]
	v_mfma_i32_16x16x64_i8 v[26:29], v[138:141], v[190:193], v[26:29]
	s_waitcnt lgkmcnt(1)
	v_mfma_i32_16x16x64_i8 v[14:17], v[130:133], v[208:211], v[14:17]
	v_mfma_i32_16x16x64_i8 v[10:13], v[138:141], v[208:211], v[10:13]
	v_mfma_i32_16x16x64_i8 v[62:65], v[134:137], v[166:169], v[62:65]
	v_mfma_i32_16x16x64_i8 v[58:61], v[142:145], v[166:169], v[58:61]
	v_mfma_i32_16x16x64_i8 v[46:49], v[134:137], v[186:189], v[46:49]
	v_mfma_i32_16x16x64_i8 v[42:45], v[142:145], v[186:189], v[42:45]
	v_mfma_i32_16x16x64_i8 v[30:33], v[134:137], v[194:197], v[30:33]
	v_mfma_i32_16x16x64_i8 v[26:29], v[142:145], v[194:197], v[26:29]
	s_waitcnt lgkmcnt(0)
	v_mfma_i32_16x16x64_i8 v[14:17], v[134:137], v[212:215], v[14:17]
	v_mfma_i32_16x16x64_i8 v[10:13], v[142:145], v[212:215], v[10:13]
	s_setprio 1
	s_setprio 0
	v_mfma_i32_16x16x64_i8 v[54:57], v[146:149], v[162:165], v[54:57]
	v_mfma_i32_16x16x64_i8 v[50:53], v[154:157], v[162:165], v[50:53]
	v_mfma_i32_16x16x64_i8 v[38:41], v[146:149], v[182:185], v[38:41]
	v_mfma_i32_16x16x64_i8 v[34:37], v[154:157], v[182:185], v[34:37]
	v_mfma_i32_16x16x64_i8 v[22:25], v[146:149], v[190:193], v[22:25]
	v_mfma_i32_16x16x64_i8 v[18:21], v[154:157], v[190:193], v[18:21]
	v_mfma_i32_16x16x64_i8 v[6:9], v[146:149], v[208:211], v[6:9]
	v_mfma_i32_16x16x64_i8 v[2:5], v[154:157], v[208:211], v[2:5]
	v_mfma_i32_16x16x64_i8 v[54:57], v[150:153], v[166:169], v[54:57]
	v_mfma_i32_16x16x64_i8 v[50:53], v[158:161], v[166:169], v[50:53]
	v_mfma_i32_16x16x64_i8 v[38:41], v[150:153], v[186:189], v[38:41]
	v_mfma_i32_16x16x64_i8 v[34:37], v[158:161], v[186:189], v[34:37]
	v_mfma_i32_16x16x64_i8 v[22:25], v[150:153], v[194:197], v[22:25]
	v_mfma_i32_16x16x64_i8 v[18:21], v[158:161], v[194:197], v[18:21]
	v_mfma_i32_16x16x64_i8 v[6:9], v[150:153], v[212:215], v[6:9]
	v_mfma_i32_16x16x64_i8 v[2:5], v[158:161], v[212:215], v[2:5]
	s_setprio 1
	s_barrier
	v_add_u32_e32 v142, 0x18000, v178
	v_add_u32_e32 v158, 0x1c000, v178
	ds_read_b128 v[130:133], v142
	ds_read_b128 v[134:137], v142 offset:1024
	ds_read_b128 v[138:141], v142 offset:2048
	ds_read_b128 v[142:145], v142 offset:3072
	ds_read_b128 v[146:149], v158
	ds_read_b128 v[150:153], v158 offset:1024
	ds_read_b128 v[154:157], v158 offset:2048
	ds_read_b128 v[158:161], v158 offset:3072
	s_mov_b32 s55, s85
	ds_read_b128 v[162:165], v177 offset:32768
	ds_read_b128 v[166:169], v177 offset:33792
	ds_read_b128 v[182:185], v177 offset:34816
	ds_read_b128 v[186:189], v177 offset:35840
	ds_read_b128 v[190:193], v177 offset:36864
	ds_read_b128 v[194:197], v177 offset:37888
	ds_read_b128 v[208:211], v177 offset:38912
	ds_read_b128 v[212:215], v177 offset:39936
	s_add_i32 s54, s54, 0x20000
	s_add_i32 m0, s55, 0x4000
	s_mov_b32 s55, s85
	buffer_load_dwordx4 v0, s[88:91], s54 offen lds
	s_add_i32 m0, s55, 0x6000
	s_nop 0
	buffer_load_dwordx4 v173, s[88:91], s54 offen lds
	s_cmp_lg_u32 s53, 0
	s_cbranch_scc1 .Lgr2
	s_waitcnt vmcnt(8)
; #define PG8_STAGE(bufoff, RS, soff, voff) do { _Pragma("unroll") for (int _i = 0; _i < 2; ++_i) \
;         __builtin_amdgcn_raw_ptr_buffer_load_lds(RS, (PG8_LAS void*)(lds + (bufoff) + sgpr_opaque(ldsw) + _i * 8192), 16, (int)(voff)[_i], (int)(soff), 0, 0); } while (0)
; #define PG8_LDA(dst, b, h) do { _Pragma("unroll") for (int m = 0; m < 4; ++m) _Pragma("unroll") for (int k = 0; k < 2; ++k) dst[m][k] = *(const PG8_LAS f16x8*)(lds + PG8_SA(b, h) + aoff + m * 2048 + k * 1024); } while (0)
; #define PG8_LDB(dst, b, h) do { _Pragma("unroll") for (int n = 0; n < 2; ++n) _Pragma("unroll") for (int k = 0; k < 2; ++k) dst[n][k] = *(const PG8_LAS f16x8*)(lds + PG8_SB(b, h) + boff + n * 2048 + k * 1024); } while (0)
; #define PG8_WAIT_L(n) asm volatile("s_waitcnt lgkmcnt(" #n ")" ::: "memory")
; #define PG8_BAR __builtin_amdgcn_s_barrier()
; #define PG8_SCHED __builtin_amdgcn_sched_barrier(0)
; template <class Epi, class Sched, bool ALIGN_EPI = false, bool SP2 = false, bool I8 = false, bool ATILED = false>
; __device__ __forceinline__ void gemm_phase(PG8_LAS unsigned char* lds, const Gemm g, const Sched& S, const Epi& E, const int wid) {
;     ...
;             PG8_LDB(B0, 0, 0); PG8_LDB(B1, 0, 1); PG8_SCHED; PG8_LDA(At, 0, 0); PG8_STAGE(PG8_SA(1, 1), rsA, a1 + hstepA, voffA);
;             PG8_WAIT_VG; PG8_WAIT_L(0); PG8_BAR; PG8_MMA(0, 0, At, B0); PG8_MMA(0, 1, At, B1); PG8_BAR; PG8_SCHED;
;             PG8_LDA(At, 0, 1); PG8_STAGE(PG8_SB(0, 0), rsB, b2, voffB); PG8_STAGE(PG8_SB(0, 1), rsB, b2 + hstep, voffB); PG8_STAGE(PG8_SA(0, 0), rsA, a2, voffA);
;             PG8_WAIT_VG; PG8_WAIT_L(0); PG8_BAR; PG8_MMA(1, 0, At, B0); PG8_MMA(1, 1, At, B1); PG8_BAR; PG8_SCHED;
;             PG8_LDB(B0, 1, 0); PG8_LDB(B1, 1, 1); PG8_SCHED; PG8_LDA(At, 1, 0); PG8_STAGE(PG8_SA(0, 1), rsA, a2 + hstepA, voffA);
;             PG8_WAIT_VG; PG8_WAIT_L(0); PG8_BAR; PG8_MMA(0, 0, At, B0); PG8_MMA(0, 1, At, B1); PG8_BAR; PG8_SCHED;
;             PG8_LDA(At, 1, 1); PG8_STAGE(PG8_SB(1, 0), rsB, b3, voffB); PG8_STAGE(PG8_SB(1, 1), rsB, b3 + hstep, voffB); PG8_STAGE(PG8_SA(1, 0), rsA, a3, voffA);
;             PG8_WAIT_VG; PG8_WAIT_L(0); PG8_BAR; PG8_MMA(1, 0, At, B0); PG8_MMA(1, 1, At, B1); PG8_BAR; PG8_SCHED;
.Lgr2:
	s_waitcnt vmcnt(24)
	s_waitcnt lgkmcnt(0)
	s_barrier
	s_setprio 0
	s_waitcnt lgkmcnt(7)
	v_mfma_i32_16x16x64_i8 v[126:129], v[130:133], v[162:165], v[126:129]
	v_mfma_i32_16x16x64_i8 v[122:125], v[138:141], v[162:165], v[122:125]
	s_waitcnt lgkmcnt(5)
	v_mfma_i32_16x16x64_i8 v[110:113], v[130:133], v[182:185], v[110:113]
	v_mfma_i32_16x16x64_i8 v[106:109], v[138:141], v[182:185], v[106:109]
	s_waitcnt lgkmcnt(3)
	v_mfma_i32_16x16x64_i8 v[94:97], v[130:133], v[190:193], v[94:97]
	v_mfma_i32_16x16x64_i8 v[90:93], v[138:141], v[190:193], v[90:93]
	s_waitcnt lgkmcnt(1)
	v_mfma_i32_16x16x64_i8 v[78:81], v[130:133], v[208:211], v[78:81]
	v_mfma_i32_16x16x64_i8 v[74:77], v[138:141], v[208:211], v[74:77]
	v_mfma_i32_16x16x64_i8 v[126:129], v[134:137], v[166:169], v[126:129]
	v_mfma_i32_16x16x64_i8 v[122:125], v[142:145], v[166:169], v[122:125]
	v_mfma_i32_16x16x64_i8 v[110:113], v[134:137], v[186:189], v[110:113]
	v_mfma_i32_16x16x64_i8 v[106:109], v[142:145], v[186:189], v[106:109]
	v_mfma_i32_16x16x64_i8 v[94:97], v[134:137], v[194:197], v[94:97]
	v_mfma_i32_16x16x64_i8 v[90:93], v[142:145], v[194:197], v[90:93]
	s_waitcnt lgkmcnt(0)
	v_mfma_i32_16x16x64_i8 v[78:81], v[134:137], v[212:215], v[78:81]
	v_mfma_i32_16x16x64_i8 v[74:77], v[142:145], v[212:215], v[74:77]
	s_setprio 1
	s_setprio 0
	v_mfma_i32_16x16x64_i8 v[118:121], v[146:149], v[162:165], v[118:121]
	v_mfma_i32_16x16x64_i8 v[114:117], v[154:157], v[162:165], v[114:117]
	v_mfma_i32_16x16x64_i8 v[102:105], v[146:149], v[182:185], v[102:105]
	v_mfma_i32_16x16x64_i8 v[98:101], v[154:157], v[182:185], v[98:101]
	v_mfma_i32_16x16x64_i8 v[86:89], v[146:149], v[190:193], v[86:89]
	v_mfma_i32_16x16x64_i8 v[82:85], v[154:157], v[190:193], v[82:85]
	v_mfma_i32_16x16x64_i8 v[70:73], v[146:149], v[208:211], v[70:73]
	v_mfma_i32_16x16x64_i8 v[66:69], v[154:157], v[208:211], v[66:69]
	v_mfma_i32_16x16x64_i8 v[118:121], v[150:153], v[166:169], v[118:121]
	v_mfma_i32_16x16x64_i8 v[114:117], v[158:161], v[166:169], v[114:117]
	v_mfma_i32_16x16x64_i8 v[102:105], v[150:153], v[186:189], v[102:105]
	v_mfma_i32_16x16x64_i8 v[98:101], v[158:161], v[186:189], v[98:101]
	v_mfma_i32_16x16x64_i8 v[86:89], v[150:153], v[194:197], v[86:89]
	v_mfma_i32_16x16x64_i8 v[82:85], v[158:161], v[194:197], v[82:85]
	v_mfma_i32_16x16x64_i8 v[70:73], v[150:153], v[212:215], v[70:73]
	v_mfma_i32_16x16x64_i8 v[66:69], v[158:161], v[212:215], v[66:69]
	s_setprio 1
	s_barrier
	s_mov_b32 s54, s85
	ds_read_b128 v[162:165], v177 offset:49152
	ds_read_b128 v[166:169], v177 offset:50176
	ds_read_b128 v[182:185], v177 offset:51200
	ds_read_b128 v[186:189], v177 offset:52224
	ds_read_b128 v[190:193], v177 offset:53248
	ds_read_b128 v[194:197], v177 offset:54272
	ds_read_b128 v[208:211], v177 offset:55296
	ds_read_b128 v[212:215], v177 offset:56320
	s_add_i32 m0, s54, 0x18000
	s_mov_b32 s54, s85
	buffer_load_dwordx4 v172, s[64:67], s52 offen lds
	s_add_i32 m0, s54, 0x1a000
	s_add_i32 s51, s51, 0xc000
	buffer_load_dwordx4 v174, s[64:67], s52 offen lds
	s_mov_b32 s52, s85
	s_add_i32 m0, s52, 0x1c000
	s_mov_b32 s52, s85
	buffer_load_dwordx4 v172, s[64:67], s51 offen lds
	s_add_i32 m0, s52, 0x1e000
	s_nop 0
	buffer_load_dwordx4 v174, s[64:67], s51 offen lds
	s_mov_b32 s51, s85
	s_add_i32 m0, s51, 0x8000
	s_mov_b32 s51, s85
	buffer_load_dwordx4 v0, s[88:91], s50 offen lds
	s_add_i32 m0, s51, 0xa000
	s_nop 0
	buffer_load_dwordx4 v173, s[88:91], s50 offen lds
	s_cmp_lg_u32 s53, 0
	s_cbranch_scc1 .Lgr3
	s_waitcnt vmcnt(8)
.Lgr3:
	s_waitcnt vmcnt(24)
	s_waitcnt lgkmcnt(0)
	s_barrier
	s_setprio 0
	s_waitcnt lgkmcnt(7)
	v_mfma_i32_16x16x64_i8 v[62:65], v[130:133], v[162:165], v[62:65]
	v_mfma_i32_16x16x64_i8 v[58:61], v[138:141], v[162:165], v[58:61]
	s_waitcnt lgkmcnt(5)
	v_mfma_i32_16x16x64_i8 v[46:49], v[130:133], v[182:185], v[46:49]
	v_mfma_i32_16x16x64_i8 v[42:45], v[138:141], v[182:185], v[42:45]
	s_waitcnt lgkmcnt(3)
	v_mfma_i32_16x16x64_i8 v[30:33], v[130:133], v[190:193], v[30:33]
	v_mfma_i32_16x16x64_i8 v[26:29], v[138:141], v[190:193], v[26:29]
	s_waitcnt lgkmcnt(1)
	v_mfma_i32_16x16x64_i8 v[14:17], v[130:133], v[208:211], v[14:17]
	v_mfma_i32_16x16x64_i8 v[10:13], v[138:141], v[208:211], v[10:13]
	v_mfma_i32_16x16x64_i8 v[62:65], v[134:137], v[166:169], v[62:65]
	v_mfma_i32_16x16x64_i8 v[58:61], v[142:145], v[166:169], v[58:61]
	v_mfma_i32_16x16x64_i8 v[46:49], v[134:137], v[186:189], v[46:49]
	v_mfma_i32_16x16x64_i8 v[42:45], v[142:145], v[186:189], v[42:45]
	v_mfma_i32_16x16x64_i8 v[30:33], v[134:137], v[194:197], v[30:33]
	v_mfma_i32_16x16x64_i8 v[26:29], v[142:145], v[194:197], v[26:29]
	s_waitcnt lgkmcnt(0)
	v_mfma_i32_16x16x64_i8 v[14:17], v[134:137], v[212:215], v[14:17]
	v_mfma_i32_16x16x64_i8 v[10:13], v[142:145], v[212:215], v[10:13]
	s_setprio 1
	s_setprio 0
	v_mfma_i32_16x16x64_i8 v[54:57], v[146:149], v[162:165], v[54:57]
	v_mfma_i32_16x16x64_i8 v[50:53], v[154:157], v[162:165], v[50:53]
	v_mfma_i32_16x16x64_i8 v[38:41], v[146:149], v[182:185], v[38:41]
	v_mfma_i32_16x16x64_i8 v[34:37], v[154:157], v[182:185], v[34:37]
	v_mfma_i32_16x16x64_i8 v[22:25], v[146:149], v[190:193], v[22:25]
	v_mfma_i32_16x16x64_i8 v[18:21], v[154:157], v[190:193], v[18:21]
	v_mfma_i32_16x16x64_i8 v[6:9], v[146:149], v[208:211], v[6:9]
	v_mfma_i32_16x16x64_i8 v[2:5], v[154:157], v[208:211], v[2:5]
	v_mfma_i32_16x16x64_i8 v[54:57], v[150:153], v[166:169], v[54:57]
	v_mfma_i32_16x16x64_i8 v[50:53], v[158:161], v[166:169], v[50:53]
	v_mfma_i32_16x16x64_i8 v[38:41], v[150:153], v[186:189], v[38:41]
	v_mfma_i32_16x16x64_i8 v[34:37], v[158:161], v[186:189], v[34:37]
	v_mfma_i32_16x16x64_i8 v[22:25], v[150:153], v[194:197], v[22:25]
	v_mfma_i32_16x16x64_i8 v[18:21], v[158:161], v[194:197], v[18:21]
	v_mfma_i32_16x16x64_i8 v[6:9], v[150:153], v[212:215], v[6:9]
	v_mfma_i32_16x16x64_i8 v[2:5], v[158:161], v[212:215], v[2:5]
	s_setprio 1
	s_barrier
	s_add_i32 s49, s49, 2
	s_addk_i32 s47, 0x100
	s_add_i32 s48, s48, 0x10000
	s_cmp_gt_u32 s49, 5
	s_cbranch_scc0 .LBB0_483
	s_and_b64 vcc, exec, s[56:57]
	s_cbranch_vccz .LBB0_486
	s_barrier

; #define PG8_STAGE(bufoff, RS, soff, voff) do { _Pragma("unroll") for (int _i = 0; _i < 2; ++_i) \
;         __builtin_amdgcn_raw_ptr_buffer_load_lds(RS, (PG8_LAS void*)(lds + (bufoff) + sgpr_opaque(ldsw) + _i * 8192), 16, (int)(voff)[_i], (int)(soff), 0, 0); } while (0)
; #define PG8_LDA(dst, b, h) do { _Pragma("unroll") for (int m = 0; m < 4; ++m) _Pragma("unroll") for (int k = 0; k < 2; ++k) dst[m][k] = *(const PG8_LAS f16x8*)(lds + PG8_SA(b, h) + aoff + m * 2048 + k * 1024); } while (0)
; #define PG8_LDB(dst, b, h) do { _Pragma("unroll") for (int n = 0; n < 2; ++n) _Pragma("unroll") for (int k = 0; k < 2; ++k) dst[n][k] = *(const PG8_LAS f16x8*)(lds + PG8_SB(b, h) + boff + n * 2048 + k * 1024); } while (0)
; #define PG8_WAIT_L(n) asm volatile("s_waitcnt lgkmcnt(" #n ")" ::: "memory")
; #define PG8_BAR __builtin_amdgcn_s_barrier()
; #define PG8_SCHED __builtin_amdgcn_sched_barrier(0)
; template <class Epi, class Sched, bool ALIGN_EPI = false, bool SP2 = false, bool I8 = false, bool ATILED = false>
; __device__ __forceinline__ void gemm_phase(PG8_LAS unsigned char* lds, const Gemm g, const Sched& S, const Epi& E, const int wid) {
;     ...
;             PG8_LDB(B0, 0, 0); PG8_LDB(B1, 0, 1); PG8_SCHED; PG8_LDA(At, 0, 0); PG8_STAGE(PG8_SA(1, 1), rsA, a1 + hstepA, voffA);
;             PG8_WAIT_VG; PG8_WAIT_L(0); PG8_BAR; PG8_MMA(0, 0, At, B0); PG8_MMA(0, 1, At, B1); PG8_BAR; PG8_SCHED;
;             PG8_LDA(At, 0, 1); PG8_STAGE(PG8_SB(0, 0), rsB, b2, voffB); PG8_STAGE(PG8_SB(0, 1), rsB, b2 + hstep, voffB); PG8_STAGE(PG8_SA(0, 0), rsA, a2, voffA);
;             PG8_WAIT_VG; PG8_WAIT_L(0); PG8_BAR; PG8_MMA(1, 0, At, B0); PG8_MMA(1, 1, At, B1); PG8_BAR; PG8_SCHED;
;             PG8_LDB(B0, 1, 0); PG8_LDB(B1, 1, 1); PG8_SCHED; PG8_LDA(At, 1, 0); PG8_STAGE(PG8_SA(0, 1), rsA, a2 + hstepA, voffA);
;             PG8_WAIT_VG; PG8_WAIT_L(0); PG8_BAR; PG8_MMA(0, 0, At, B0); PG8_MMA(0, 1, At, B1); PG8_BAR; PG8_SCHED;
;             PG8_LDA(At, 1, 1); PG8_STAGE(PG8_SB(1, 0), rsB, b3, voffB); PG8_STAGE(PG8_SB(1, 1), rsB, b3 + hstep, voffB); PG8_STAGE(PG8_SA(1, 0), rsA, a3, voffA);
;             PG8_WAIT_VG; PG8_WAIT_L(0); PG8_BAR; PG8_MMA(1, 0, At, B0); PG8_MMA(1, 1, At, B1); PG8_BAR; PG8_SCHED;
.Lgr4:
	s_waitcnt vmcnt(24)
	s_waitcnt lgkmcnt(0)
	s_barrier
	s_setprio 0
	s_waitcnt lgkmcnt(0)
	v_mfma_f32_16x16x32_f16 v[126:129], v[138:141], v[170:173], v[126:129]
	v_mfma_f32_16x16x32_f16 v[122:125], v[146:149], v[170:173], v[122:125]
	v_mfma_f32_16x16x32_f16 v[118:121], v[138:141], v[178:181], v[118:121]
	v_mfma_f32_16x16x32_f16 v[114:117], v[146:149], v[178:181], v[114:117]
	v_mfma_f32_16x16x32_f16 v[102:105], v[138:141], v[186:189], v[102:105]
	v_mfma_f32_16x16x32_f16 v[98:101], v[146:149], v[186:189], v[98:101]
	v_mfma_f32_16x16x32_f16 v[86:89], v[138:141], v[194:197], v[86:89]
	v_mfma_f32_16x16x32_f16 v[82:85], v[146:149], v[194:197], v[82:85]
	v_mfma_f32_16x16x32_f16 v[126:129], v[142:145], v[174:177], v[126:129]
	v_mfma_f32_16x16x32_f16 v[122:125], v[150:153], v[174:177], v[122:125]
	v_mfma_f32_16x16x32_f16 v[118:121], v[142:145], v[182:185], v[118:121]
	v_mfma_f32_16x16x32_f16 v[114:117], v[150:153], v[182:185], v[114:117]
	v_mfma_f32_16x16x32_f16 v[102:105], v[142:145], v[190:193], v[102:105]
	v_mfma_f32_16x16x32_f16 v[98:101], v[150:153], v[190:193], v[98:101]
	v_mfma_f32_16x16x32_f16 v[86:89], v[142:145], v[208:211], v[86:89]
	v_mfma_f32_16x16x32_f16 v[82:85], v[150:153], v[208:211], v[82:85]
	s_setprio 1
	s_setprio 0
	v_mfma_f32_16x16x32_f16 v[110:113], v[154:157], v[170:173], v[110:113]
	v_mfma_f32_16x16x32_f16 v[106:109], v[162:165], v[170:173], v[106:109]
	v_mfma_f32_16x16x32_f16 v[94:97], v[154:157], v[178:181], v[94:97]
	v_mfma_f32_16x16x32_f16 v[90:93], v[162:165], v[178:181], v[90:93]
	v_mfma_f32_16x16x32_f16 v[78:81], v[154:157], v[186:189], v[78:81]
	v_mfma_f32_16x16x32_f16 v[74:77], v[162:165], v[186:189], v[74:77]
	v_mfma_f32_16x16x32_f16 v[70:73], v[154:157], v[194:197], v[70:73]
	v_mfma_f32_16x16x32_f16 v[66:69], v[162:165], v[194:197], v[66:69]
	v_mfma_f32_16x16x32_f16 v[110:113], v[158:161], v[174:177], v[110:113]
	v_mfma_f32_16x16x32_f16 v[106:109], v[166:169], v[174:177], v[106:109]
	v_mfma_f32_16x16x32_f16 v[94:97], v[158:161], v[182:185], v[94:97]
	v_mfma_f32_16x16x32_f16 v[90:93], v[166:169], v[182:185], v[90:93]
	v_mfma_f32_16x16x32_f16 v[78:81], v[158:161], v[190:193], v[78:81]
	v_mfma_f32_16x16x32_f16 v[74:77], v[166:169], v[190:193], v[74:77]
	v_mfma_f32_16x16x32_f16 v[70:73], v[158:161], v[208:211], v[70:73]
	v_mfma_f32_16x16x32_f16 v[66:69], v[166:169], v[208:211], v[66:69]
	s_setprio 1
	s_barrier
	s_mov_b32 s38, s85
	ds_read_b128 v[170:173], v134 offset:16384
	ds_read_b128 v[174:177], v134 offset:17408
	ds_read_b128 v[178:181], v134 offset:18432
	ds_read_b128 v[182:185], v134 offset:19456
	ds_read_b128 v[186:189], v134 offset:20480
	ds_read_b128 v[190:193], v134 offset:21504
	ds_read_b128 v[194:197], v134 offset:22528
	ds_read_b128 v[208:211], v134 offset:23552
	s_add_i32 m0, s38, 0x10000
	s_mov_b32 s38, s66
	s_mov_b32 s39, s67
	s_mov_b32 s71, s85
	buffer_load_dwordx4 v130, s[36:39], s70 offen lds
	s_add_i32 m0, s71, 0x12000
	s_mov_b32 s71, s85
	buffer_load_dwordx4 v132, s[36:39], s70 offen lds
	s_add_i32 s70, s70, s44
	s_add_i32 m0, s71, 0x14000
	s_mov_b32 s71, s85
	buffer_load_dwordx4 v130, s[36:39], s70 offen lds
	s_add_i32 m0, s71, 0x16000
	s_nop 0
	buffer_load_dwordx4 v132, s[36:39], s70 offen lds
	s_mov_b32 s70, s85
	s_mov_b32 m0, s70
	s_mov_b32 s70, s85
	buffer_load_dwordx4 v0, s[64:67], s69 offen lds
	s_add_i32 m0, s70, 0x2000
	s_nop 0
	buffer_load_dwordx4 v131, s[64:67], s69 offen lds
	s_cmp_lg_u32 s63, 0
	s_cbranch_scc1 .Lgr5
	s_waitcnt vmcnt(8)
.Lgr5:
	s_waitcnt vmcnt(24)
	s_waitcnt lgkmcnt(0)
	s_barrier
	s_setprio 0
	s_waitcnt lgkmcnt(0)
	v_mfma_f32_16x16x32_f16 v[62:65], v[138:141], v[170:173], v[62:65]
	v_mfma_f32_16x16x32_f16 v[58:61], v[146:149], v[170:173], v[58:61]
	v_mfma_f32_16x16x32_f16 v[54:57], v[138:141], v[178:181], v[54:57]
	v_mfma_f32_16x16x32_f16 v[50:53], v[146:149], v[178:181], v[50:53]
	v_mfma_f32_16x16x32_f16 v[38:41], v[138:141], v[186:189], v[38:41]
	v_mfma_f32_16x16x32_f16 v[34:37], v[146:149], v[186:189], v[34:37]
	v_mfma_f32_16x16x32_f16 v[22:25], v[138:141], v[194:197], v[22:25]
	v_mfma_f32_16x16x32_f16 v[18:21], v[146:149], v[194:197], v[18:21]
	v_mfma_f32_16x16x32_f16 v[62:65], v[142:145], v[174:177], v[62:65]
	v_mfma_f32_16x16x32_f16 v[58:61], v[150:153], v[174:177], v[58:61]
	v_mfma_f32_16x16x32_f16 v[54:57], v[142:145], v[182:185], v[54:57]
	v_mfma_f32_16x16x32_f16 v[50:53], v[150:153], v[182:185], v[50:53]
	v_mfma_f32_16x16x32_f16 v[38:41], v[142:145], v[190:193], v[38:41]
	v_mfma_f32_16x16x32_f16 v[34:37], v[150:153], v[190:193], v[34:37]
	v_mfma_f32_16x16x32_f16 v[22:25], v[142:145], v[208:211], v[22:25]
	v_mfma_f32_16x16x32_f16 v[18:21], v[150:153], v[208:211], v[18:21]
	s_setprio 1
	s_setprio 0
	v_mfma_f32_16x16x32_f16 v[46:49], v[154:157], v[170:173], v[46:49]
	v_mfma_f32_16x16x32_f16 v[42:45], v[162:165], v[170:173], v[42:45]
	v_mfma_f32_16x16x32_f16 v[30:33], v[154:157], v[178:181], v[30:33]
	v_mfma_f32_16x16x32_f16 v[26:29], v[162:165], v[178:181], v[26:29]
	v_mfma_f32_16x16x32_f16 v[14:17], v[154:157], v[186:189], v[14:17]
	v_mfma_f32_16x16x32_f16 v[10:13], v[162:165], v[186:189], v[10:13]
	v_mfma_f32_16x16x32_f16 v[6:9], v[154:157], v[194:197], v[6:9]
	v_mfma_f32_16x16x32_f16 v[2:5], v[162:165], v[194:197], v[2:5]
	v_mfma_f32_16x16x32_f16 v[46:49], v[158:161], v[174:177], v[46:49]
	v_mfma_f32_16x16x32_f16 v[42:45], v[166:169], v[174:177], v[42:45]
	v_mfma_f32_16x16x32_f16 v[30:33], v[158:161], v[182:185], v[30:33]
	v_mfma_f32_16x16x32_f16 v[26:29], v[166:169], v[182:185], v[26:29]
	v_mfma_f32_16x16x32_f16 v[14:17], v[158:161], v[190:193], v[14:17]
	v_mfma_f32_16x16x32_f16 v[10:13], v[166:169], v[190:193], v[10:13]
	v_mfma_f32_16x16x32_f16 v[6:9], v[158:161], v[208:211], v[6:9]
	v_mfma_f32_16x16x32_f16 v[2:5], v[166:169], v[208:211], v[2:5]
	s_setprio 1
	s_barrier
	v_add_u32_e32 v137, 0x18000, v135
	ds_read_b128 v[138:141], v137
	ds_read_b128 v[142:145], v137 offset:1024
	ds_read_b128 v[146:149], v137 offset:2048
	ds_read_b128 v[150:153], v137 offset:3072
	v_add_u32_e32 v137, 0x1c000, v135
	ds_read_b128 v[154:157], v137
	ds_read_b128 v[158:161], v137 offset:1024
	ds_read_b128 v[162:165], v137 offset:2048
	ds_read_b128 v[166:169], v137 offset:3072
	s_mov_b32 s70, s85
	ds_read_b128 v[170:173], v134 offset:32768
	ds_read_b128 v[174:177], v134 offset:33792
	ds_read_b128 v[178:181], v134 offset:34816
	ds_read_b128 v[182:185], v134 offset:35840
	ds_read_b128 v[186:189], v134 offset:36864
	ds_read_b128 v[190:193], v134 offset:37888
	ds_read_b128 v[194:197], v134 offset:38912
	ds_read_b128 v[208:211], v134 offset:39936
	s_add_i32 s69, s69, s44
	s_add_i32 m0, s70, 0x4000
	s_mov_b32 s70, s85
	buffer_load_dwordx4 v0, s[64:67], s69 offen lds
	s_add_i32 m0, s70, 0x6000
	s_nop 0
	buffer_load_dwordx4 v131, s[64:67], s69 offen lds
	s_cmp_lg_u32 s63, 0
	s_cbranch_scc1 .Lgr6
	s_waitcnt vmcnt(8)
; #define PG8_STAGE(bufoff, RS, soff, voff) do { _Pragma("unroll") for (int _i = 0; _i < 2; ++_i) \
;         __builtin_amdgcn_raw_ptr_buffer_load_lds(RS, (PG8_LAS void*)(lds + (bufoff) + sgpr_opaque(ldsw) + _i * 8192), 16, (int)(voff)[_i], (int)(soff), 0, 0); } while (0)
; #define PG8_LDA(dst, b, h) do { _Pragma("unroll") for (int m = 0; m < 4; ++m) _Pragma("unroll") for (int k = 0; k < 2; ++k) dst[m][k] = *(const PG8_LAS f16x8*)(lds + PG8_SA(b, h) + aoff + m * 2048 + k * 1024); } while (0)
; #define PG8_LDB(dst, b, h) do { _Pragma("unroll") for (int n = 0; n < 2; ++n) _Pragma("unroll") for (int k = 0; k < 2; ++k) dst[n][k] = *(const PG8_LAS f16x8*)(lds + PG8_SB(b, h) + boff + n * 2048 + k * 1024); } while (0)
; #define PG8_WAIT_L(n) asm volatile("s_waitcnt lgkmcnt(" #n ")" ::: "memory")
; #define PG8_BAR __builtin_amdgcn_s_barrier()
; #define PG8_SCHED __builtin_amdgcn_sched_barrier(0)
; template <class Epi, class Sched, bool ALIGN_EPI = false, bool SP2 = false, bool I8 = false, bool ATILED = false>
; __device__ __forceinline__ void gemm_phase(PG8_LAS unsigned char* lds, const Gemm g, const Sched& S, const Epi& E, const int wid) {
;     ...
;             PG8_LDB(B0, 0, 0); PG8_LDB(B1, 0, 1); PG8_SCHED; PG8_LDA(At, 0, 0); PG8_STAGE(PG8_SA(1, 1), rsA, a1 + hstepA, voffA);
;             PG8_WAIT_VG; PG8_WAIT_L(0); PG8_BAR; PG8_MMA(0, 0, At, B0); PG8_MMA(0, 1, At, B1); PG8_BAR; PG8_SCHED;
;             PG8_LDA(At, 0, 1); PG8_STAGE(PG8_SB(0, 0), rsB, b2, voffB); PG8_STAGE(PG8_SB(0, 1), rsB, b2 + hstep, voffB); PG8_STAGE(PG8_SA(0, 0), rsA, a2, voffA);
;             PG8_WAIT_VG; PG8_WAIT_L(0); PG8_BAR; PG8_MMA(1, 0, At, B0); PG8_MMA(1, 1, At, B1); PG8_BAR; PG8_SCHED;
;             PG8_LDB(B0, 1, 0); PG8_LDB(B1, 1, 1); PG8_SCHED; PG8_LDA(At, 1, 0); PG8_STAGE(PG8_SA(0, 1), rsA, a2 + hstepA, voffA);
;             PG8_WAIT_VG; PG8_WAIT_L(0); PG8_BAR; PG8_MMA(0, 0, At, B0); PG8_MMA(0, 1, At, B1); PG8_BAR; PG8_SCHED;
;             PG8_LDA(At, 1, 1); PG8_STAGE(PG8_SB(1, 0), rsB, b3, voffB); PG8_STAGE(PG8_SB(1, 1), rsB, b3 + hstep, voffB); PG8_STAGE(PG8_SA(1, 0), rsA, a3, voffA);
;             PG8_WAIT_VG; PG8_WAIT_L(0); PG8_BAR; PG8_MMA(1, 0, At, B0); PG8_MMA(1, 1, At, B1); PG8_BAR; PG8_SCHED;
.Lgr6:
	s_waitcnt vmcnt(24)
	s_waitcnt lgkmcnt(0)
	s_barrier
	s_setprio 0
	s_waitcnt lgkmcnt(0)
	v_mfma_f32_16x16x32_f16 v[126:129], v[138:141], v[170:173], v[126:129]
	v_mfma_f32_16x16x32_f16 v[122:125], v[146:149], v[170:173], v[122:125]
	v_mfma_f32_16x16x32_f16 v[118:121], v[138:141], v[178:181], v[118:121]
	v_mfma_f32_16x16x32_f16 v[114:117], v[146:149], v[178:181], v[114:117]
	v_mfma_f32_16x16x32_f16 v[102:105], v[138:141], v[186:189], v[102:105]
	v_mfma_f32_16x16x32_f16 v[98:101], v[146:149], v[186:189], v[98:101]
	v_mfma_f32_16x16x32_f16 v[86:89], v[138:141], v[194:197], v[86:89]
	v_mfma_f32_16x16x32_f16 v[82:85], v[146:149], v[194:197], v[82:85]
	v_mfma_f32_16x16x32_f16 v[126:129], v[142:145], v[174:177], v[126:129]
	v_mfma_f32_16x16x32_f16 v[122:125], v[150:153], v[174:177], v[122:125]
	v_mfma_f32_16x16x32_f16 v[118:121], v[142:145], v[182:185], v[118:121]
	v_mfma_f32_16x16x32_f16 v[114:117], v[150:153], v[182:185], v[114:117]
	v_mfma_f32_16x16x32_f16 v[102:105], v[142:145], v[190:193], v[102:105]
	v_mfma_f32_16x16x32_f16 v[98:101], v[150:153], v[190:193], v[98:101]
	v_mfma_f32_16x16x32_f16 v[86:89], v[142:145], v[208:211], v[86:89]
	v_mfma_f32_16x16x32_f16 v[82:85], v[150:153], v[208:211], v[82:85]
	s_setprio 1
	s_setprio 0
	v_mfma_f32_16x16x32_f16 v[110:113], v[154:157], v[170:173], v[110:113]
	v_mfma_f32_16x16x32_f16 v[106:109], v[162:165], v[170:173], v[106:109]
	v_mfma_f32_16x16x32_f16 v[94:97], v[154:157], v[178:181], v[94:97]
	v_mfma_f32_16x16x32_f16 v[90:93], v[162:165], v[178:181], v[90:93]
	v_mfma_f32_16x16x32_f16 v[78:81], v[154:157], v[186:189], v[78:81]
	v_mfma_f32_16x16x32_f16 v[74:77], v[162:165], v[186:189], v[74:77]
	v_mfma_f32_16x16x32_f16 v[70:73], v[154:157], v[194:197], v[70:73]
	v_mfma_f32_16x16x32_f16 v[66:69], v[162:165], v[194:197], v[66:69]
	v_mfma_f32_16x16x32_f16 v[110:113], v[158:161], v[174:177], v[110:113]
	v_mfma_f32_16x16x32_f16 v[106:109], v[166:169], v[174:177], v[106:109]
	v_mfma_f32_16x16x32_f16 v[94:97], v[158:161], v[182:185], v[94:97]
	v_mfma_f32_16x16x32_f16 v[90:93], v[166:169], v[182:185], v[90:93]
	v_mfma_f32_16x16x32_f16 v[78:81], v[158:161], v[190:193], v[78:81]
	v_mfma_f32_16x16x32_f16 v[74:77], v[166:169], v[190:193], v[74:77]
	v_mfma_f32_16x16x32_f16 v[70:73], v[158:161], v[208:211], v[70:73]
	v_mfma_f32_16x16x32_f16 v[66:69], v[166:169], v[208:211], v[66:69]
	s_setprio 1
	s_barrier
	s_mov_b32 s69, s85
	ds_read_b128 v[170:173], v134 offset:49152
	ds_read_b128 v[174:177], v134 offset:50176
	ds_read_b128 v[178:181], v134 offset:51200
	ds_read_b128 v[182:185], v134 offset:52224
	ds_read_b128 v[186:189], v134 offset:53248
	ds_read_b128 v[190:193], v134 offset:54272
	ds_read_b128 v[194:197], v134 offset:55296
	ds_read_b128 v[208:211], v134 offset:56320
	s_add_i32 m0, s69, 0x18000
	s_mov_b32 s69, s85
	buffer_load_dwordx4 v130, s[36:39], s62 offen lds
	s_add_i32 m0, s69, 0x1a000
	s_mov_b32 s69, s85
	buffer_load_dwordx4 v132, s[36:39], s62 offen lds
	s_add_i32 s62, s62, s44
	s_add_i32 m0, s69, 0x1c000
	s_mov_b32 s69, s85
	buffer_load_dwordx4 v130, s[36:39], s62 offen lds
	s_add_i32 m0, s69, 0x1e000
	s_nop 0
	buffer_load_dwordx4 v132, s[36:39], s62 offen lds
	s_mov_b32 s38, s85
	s_add_i32 m0, s38, 0x8000
	s_mov_b32 s38, s85
	buffer_load_dwordx4 v0, s[64:67], s61 offen lds
	s_add_i32 m0, s38, 0xa000
	s_nop 0
	buffer_load_dwordx4 v131, s[64:67], s61 offen lds
	s_cmp_lg_u32 s63, 0
	s_cbranch_scc1 .Lgr7
	s_waitcnt vmcnt(8)
.Lgr7:
	s_waitcnt vmcnt(24)
	s_waitcnt lgkmcnt(0)
	s_barrier
	s_setprio 0
	s_waitcnt lgkmcnt(0)
	v_mfma_f32_16x16x32_f16 v[62:65], v[138:141], v[170:173], v[62:65]
	v_mfma_f32_16x16x32_f16 v[58:61], v[146:149], v[170:173], v[58:61]
	v_mfma_f32_16x16x32_f16 v[54:57], v[138:141], v[178:181], v[54:57]
	v_mfma_f32_16x16x32_f16 v[50:53], v[146:149], v[178:181], v[50:53]
	v_mfma_f32_16x16x32_f16 v[38:41], v[138:141], v[186:189], v[38:41]
	v_mfma_f32_16x16x32_f16 v[34:37], v[146:149], v[186:189], v[34:37]
	v_mfma_f32_16x16x32_f16 v[22:25], v[138:141], v[194:197], v[22:25]
	v_mfma_f32_16x16x32_f16 v[18:21], v[146:149], v[194:197], v[18:21]
	v_mfma_f32_16x16x32_f16 v[62:65], v[142:145], v[174:177], v[62:65]
	v_mfma_f32_16x16x32_f16 v[58:61], v[150:153], v[174:177], v[58:61]
	v_mfma_f32_16x16x32_f16 v[54:57], v[142:145], v[182:185], v[54:57]
	v_mfma_f32_16x16x32_f16 v[50:53], v[150:153], v[182:185], v[50:53]
	v_mfma_f32_16x16x32_f16 v[38:41], v[142:145], v[190:193], v[38:41]
	v_mfma_f32_16x16x32_f16 v[34:37], v[150:153], v[190:193], v[34:37]
	v_mfma_f32_16x16x32_f16 v[22:25], v[142:145], v[208:211], v[22:25]
	v_mfma_f32_16x16x32_f16 v[18:21], v[150:153], v[208:211], v[18:21]
	s_setprio 1
	s_setprio 0
	v_mfma_f32_16x16x32_f16 v[46:49], v[154:157], v[170:173], v[46:49]
	v_mfma_f32_16x16x32_f16 v[42:45], v[162:165], v[170:173], v[42:45]
	v_mfma_f32_16x16x32_f16 v[30:33], v[154:157], v[178:181], v[30:33]
	v_mfma_f32_16x16x32_f16 v[26:29], v[162:165], v[178:181], v[26:29]
	v_mfma_f32_16x16x32_f16 v[14:17], v[154:157], v[186:189], v[14:17]
	v_mfma_f32_16x16x32_f16 v[10:13], v[162:165], v[186:189], v[10:13]
	v_mfma_f32_16x16x32_f16 v[6:9], v[154:157], v[194:197], v[6:9]
	v_mfma_f32_16x16x32_f16 v[2:5], v[162:165], v[194:197], v[2:5]
	v_mfma_f32_16x16x32_f16 v[46:49], v[158:161], v[174:177], v[46:49]
	v_mfma_f32_16x16x32_f16 v[42:45], v[166:169], v[174:177], v[42:45]
	v_mfma_f32_16x16x32_f16 v[30:33], v[158:161], v[182:185], v[30:33]
	v_mfma_f32_16x16x32_f16 v[26:29], v[166:169], v[182:185], v[26:29]
	v_mfma_f32_16x16x32_f16 v[14:17], v[158:161], v[190:193], v[14:17]
	v_mfma_f32_16x16x32_f16 v[10:13], v[166:169], v[190:193], v[10:13]
	v_mfma_f32_16x16x32_f16 v[6:9], v[158:161], v[208:211], v[6:9]
	v_mfma_f32_16x16x32_f16 v[2:5], v[166:169], v[208:211], v[2:5]
	s_setprio 1
	s_barrier
	s_add_i32 s58, s58, 2
	s_addk_i32 s59, 0x100
	s_addk_i32 s60, 0x100
	s_cmp_ge_u32 s58, s45
	s_cbranch_scc0 .LBB0_1132
	s_and_b64 vcc, exec, s[56:57]
	s_cbranch_vccz .LBB0_1135
	s_barrier

; #define PG8_STAGE(bufoff, RS, soff, voff) do { _Pragma("unroll") for (int _i = 0; _i < 2; ++_i) \
;         __builtin_amdgcn_raw_ptr_buffer_load_lds(RS, (PG8_LAS void*)(lds + (bufoff) + sgpr_opaque(ldsw) + _i * 8192), 16, (int)(voff)[_i], (int)(soff), 0, 0); } while (0)
; #define PG8_LDA(dst, b, h) do { _Pragma("unroll") for (int m = 0; m < 4; ++m) _Pragma("unroll") for (int k = 0; k < 2; ++k) dst[m][k] = *(const PG8_LAS f16x8*)(lds + PG8_SA(b, h) + aoff + m * 2048 + k * 1024); } while (0)
; #define PG8_LDB(dst, b, h) do { _Pragma("unroll") for (int n = 0; n < 2; ++n) _Pragma("unroll") for (int k = 0; k < 2; ++k) dst[n][k] = *(const PG8_LAS f16x8*)(lds + PG8_SB(b, h) + boff + n * 2048 + k * 1024); } while (0)
; #define PG8_WAIT_L(n) asm volatile("s_waitcnt lgkmcnt(" #n ")" ::: "memory")
; #define PG8_BAR __builtin_amdgcn_s_barrier()
; #define PG8_SCHED __builtin_amdgcn_sched_barrier(0)
; template <class Epi, class Sched, bool ALIGN_EPI = false, bool SP2 = false, bool I8 = false, bool ATILED = false>
; __device__ __forceinline__ void gemm_phase(PG8_LAS unsigned char* lds, const Gemm g, const Sched& S, const Epi& E, const int wid) {
;     ...
;             PG8_LDB(B0, 0, 0); PG8_LDB(B1, 0, 1); PG8_SCHED; PG8_LDA(At, 0, 0); PG8_STAGE(PG8_SA(1, 1), rsA, a1 + hstepA, voffA);
;             PG8_WAIT_VG; PG8_WAIT_L(0); PG8_BAR; PG8_MMA(0, 0, At, B0); PG8_MMA(0, 1, At, B1); PG8_BAR; PG8_SCHED;
;             PG8_LDA(At, 0, 1); PG8_STAGE(PG8_SB(0, 0), rsB, b2, voffB); PG8_STAGE(PG8_SB(0, 1), rsB, b2 + hstep, voffB); PG8_STAGE(PG8_SA(0, 0), rsA, a2, voffA);
;             PG8_WAIT_VG; PG8_WAIT_L(0); PG8_BAR; PG8_MMA(1, 0, At, B0); PG8_MMA(1, 1, At, B1); PG8_BAR; PG8_SCHED;
;             PG8_LDB(B0, 1, 0); PG8_LDB(B1, 1, 1); PG8_SCHED; PG8_LDA(At, 1, 0); PG8_STAGE(PG8_SA(0, 1), rsA, a2 + hstepA, voffA);
;             PG8_WAIT_VG; PG8_WAIT_L(0); PG8_BAR; PG8_MMA(0, 0, At, B0); PG8_MMA(0, 1, At, B1); PG8_BAR; PG8_SCHED;
;             PG8_LDA(At, 1, 1); PG8_STAGE(PG8_SB(1, 0), rsB, b3, voffB); PG8_STAGE(PG8_SB(1, 1), rsB, b3 + hstep, voffB); PG8_STAGE(PG8_SA(1, 0), rsA, a3, voffA);
;             PG8_WAIT_VG; PG8_WAIT_L(0); PG8_BAR; PG8_MMA(1, 0, At, B0); PG8_MMA(1, 1, At, B1); PG8_BAR; PG8_SCHED;
.Lgr8:
	s_waitcnt vmcnt(36)
	s_waitcnt lgkmcnt(0)
	s_barrier
	s_setprio 0
	s_waitcnt lgkmcnt(7)
	v_mfma_i32_16x16x64_i8 v[182:185], v[26:29], v[58:61], v[182:185]
	v_mfma_i32_16x16x64_i8 v[178:181], v[34:37], v[58:61], v[178:181]
	s_waitcnt lgkmcnt(5)
	v_mfma_i32_16x16x64_i8 v[158:161], v[26:29], v[66:69], v[158:161]
	v_mfma_i32_16x16x64_i8 v[154:157], v[34:37], v[66:69], v[154:157]
	s_waitcnt lgkmcnt(3)
	v_mfma_i32_16x16x64_i8 v[142:145], v[26:29], v[162:165], v[142:145]
	v_mfma_i32_16x16x64_i8 v[138:141], v[34:37], v[162:165], v[138:141]
	s_waitcnt lgkmcnt(1)
	v_mfma_i32_16x16x64_i8 v[126:129], v[26:29], v[186:189], v[126:129]
	v_mfma_i32_16x16x64_i8 v[122:125], v[34:37], v[186:189], v[122:125]
	v_mfma_i32_16x16x64_i8 v[182:185], v[30:33], v[62:65], v[182:185]
	v_mfma_i32_16x16x64_i8 v[178:181], v[38:41], v[62:65], v[178:181]
	v_mfma_i32_16x16x64_i8 v[158:161], v[30:33], v[70:73], v[158:161]
	v_mfma_i32_16x16x64_i8 v[154:157], v[38:41], v[70:73], v[154:157]
	v_mfma_i32_16x16x64_i8 v[142:145], v[30:33], v[174:177], v[142:145]
	v_mfma_i32_16x16x64_i8 v[138:141], v[38:41], v[174:177], v[138:141]
	s_waitcnt lgkmcnt(0)
	v_mfma_i32_16x16x64_i8 v[126:129], v[30:33], v[190:193], v[126:129]
	v_mfma_i32_16x16x64_i8 v[122:125], v[38:41], v[190:193], v[122:125]
	s_setprio 1
	s_setprio 0
	v_mfma_i32_16x16x64_i8 v[170:173], v[42:45], v[58:61], v[170:173]
	v_mfma_i32_16x16x64_i8 v[58:61], v[50:53], v[58:61], v[166:169]
	v_mfma_i32_16x16x64_i8 v[170:173], v[46:49], v[62:65], v[170:173]
	v_mfma_i32_16x16x64_i8 v[58:61], v[54:57], v[62:65], v[58:61]
	v_mfma_i32_16x16x64_i8 v[62:65], v[42:45], v[66:69], v[150:153]
	v_mfma_i32_16x16x64_i8 v[66:69], v[50:53], v[66:69], v[146:149]
	v_mfma_i32_16x16x64_i8 v[130:133], v[50:53], v[162:165], v[130:133]
	v_mfma_i32_16x16x64_i8 v[118:121], v[42:45], v[186:189], v[118:121]
	v_mfma_i32_16x16x64_i8 v[114:117], v[50:53], v[186:189], v[114:117]
	v_mfma_i32_16x16x64_i8 v[62:65], v[46:49], v[70:73], v[62:65]
	v_mfma_i32_16x16x64_i8 v[66:69], v[54:57], v[70:73], v[66:69]
	v_mfma_i32_16x16x64_i8 v[70:73], v[42:45], v[162:165], v[134:137]
	v_mfma_i32_16x16x64_i8 v[130:133], v[54:57], v[174:177], v[130:133]
	v_mfma_i32_16x16x64_i8 v[118:121], v[46:49], v[190:193], v[118:121]
	v_mfma_i32_16x16x64_i8 v[114:117], v[54:57], v[190:193], v[114:117]
	v_mfma_i32_16x16x64_i8 v[70:73], v[46:49], v[174:177], v[70:73]
	s_setprio 1
	s_barrier
	s_mov_b32 s62, s85
	ds_read_b128 v[134:137], v209 offset:16384
	ds_read_b128 v[146:149], v209 offset:17408
	ds_read_b128 v[150:153], v209 offset:18432
	ds_read_b128 v[162:165], v209 offset:19456
	ds_read_b128 v[166:169], v209 offset:20480
	ds_read_b128 v[174:177], v209 offset:21504
	ds_read_b128 v[186:189], v209 offset:22528
	ds_read_b128 v[190:193], v209 offset:23552
	s_add_i32 m0, s62, 0x10000
	s_mov_b32 s62, s85
	buffer_load_dwordx4 v194, s[64:67], s52 offen lds
	s_add_i32 m0, s62, 0x12000
	s_mov_b32 s63, s85
	buffer_load_dwordx4 v196, s[64:67], s52 offen lds
	s_add_i32 s62, s52, 0x4000
	s_add_i32 m0, s63, 0x14000
	s_mov_b32 s63, s85
	buffer_load_dwordx4 v194, s[64:67], s62 offen lds
	s_add_i32 m0, s63, 0x16000
	s_nop 0
	buffer_load_dwordx4 v196, s[64:67], s62 offen lds
	s_mov_b32 s62, s85
	s_mov_b32 m0, s62
	s_mov_b32 s62, s85
	buffer_load_dwordx4 v0, s[88:91], s69 offen lds
	s_add_i32 m0, s62, 0x2000
	s_nop 0
	buffer_load_dwordx4 v195, s[88:91], s69 offen lds
	s_cmp_lg_u32 s61, 0
	s_cbranch_scc1 .Lgr9
	s_waitcnt vmcnt(8)
.Lgr9:
	s_waitcnt vmcnt(36)
	s_waitcnt lgkmcnt(0)
	s_barrier
	s_setprio 0
	s_waitcnt lgkmcnt(7)
	v_mfma_i32_16x16x64_i8 v[110:113], v[26:29], v[134:137], v[110:113]
	v_mfma_i32_16x16x64_i8 v[106:109], v[34:37], v[134:137], v[106:109]
	s_waitcnt lgkmcnt(5)
	v_mfma_i32_16x16x64_i8 v[94:97], v[26:29], v[150:153], v[94:97]
	v_mfma_i32_16x16x64_i8 v[90:93], v[34:37], v[150:153], v[90:93]
	s_waitcnt lgkmcnt(3)
	v_mfma_i32_16x16x64_i8 v[78:81], v[26:29], v[166:169], v[78:81]
	v_mfma_i32_16x16x64_i8 v[74:77], v[34:37], v[166:169], v[74:77]
	s_waitcnt lgkmcnt(1)
	v_mfma_i32_16x16x64_i8 v[14:17], v[26:29], v[186:189], v[14:17]
	v_mfma_i32_16x16x64_i8 v[10:13], v[34:37], v[186:189], v[10:13]
	v_mfma_i32_16x16x64_i8 v[110:113], v[30:33], v[146:149], v[110:113]
	v_mfma_i32_16x16x64_i8 v[106:109], v[38:41], v[146:149], v[106:109]
	v_mfma_i32_16x16x64_i8 v[94:97], v[30:33], v[162:165], v[94:97]
	v_mfma_i32_16x16x64_i8 v[90:93], v[38:41], v[162:165], v[90:93]
	v_mfma_i32_16x16x64_i8 v[78:81], v[30:33], v[174:177], v[78:81]
	v_mfma_i32_16x16x64_i8 v[74:77], v[38:41], v[174:177], v[74:77]
	s_waitcnt lgkmcnt(0)
	v_mfma_i32_16x16x64_i8 v[14:17], v[30:33], v[190:193], v[14:17]
	v_mfma_i32_16x16x64_i8 v[10:13], v[38:41], v[190:193], v[10:13]
	s_setprio 1
	s_setprio 0
	v_mfma_i32_16x16x64_i8 v[22:25], v[42:45], v[166:169], v[22:25]
	v_mfma_i32_16x16x64_i8 v[18:21], v[50:53], v[166:169], v[18:21]
	v_mfma_i32_16x16x64_i8 v[6:9], v[42:45], v[186:189], v[6:9]
	v_mfma_i32_16x16x64_i8 v[2:5], v[50:53], v[186:189], v[2:5]
	v_mfma_i32_16x16x64_i8 v[26:29], v[42:45], v[134:137], v[102:105]
	v_mfma_i32_16x16x64_i8 v[30:33], v[50:53], v[134:137], v[98:101]
	v_mfma_i32_16x16x64_i8 v[34:37], v[42:45], v[150:153], v[86:89]
	v_mfma_i32_16x16x64_i8 v[38:41], v[50:53], v[150:153], v[82:85]
	v_mfma_i32_16x16x64_i8 v[22:25], v[46:49], v[174:177], v[22:25]
	v_mfma_i32_16x16x64_i8 v[18:21], v[54:57], v[174:177], v[18:21]
	v_mfma_i32_16x16x64_i8 v[6:9], v[46:49], v[190:193], v[6:9]
	v_mfma_i32_16x16x64_i8 v[2:5], v[54:57], v[190:193], v[2:5]
	v_mfma_i32_16x16x64_i8 v[26:29], v[46:49], v[146:149], v[26:29]
	v_mfma_i32_16x16x64_i8 v[30:33], v[54:57], v[146:149], v[30:33]
	v_mfma_i32_16x16x64_i8 v[34:37], v[46:49], v[162:165], v[34:37]
	v_mfma_i32_16x16x64_i8 v[38:41], v[54:57], v[162:165], v[38:41]
	s_setprio 1
	s_barrier
	v_add_u32_e32 v54, 0x18000, v210
	v_add_u32_e32 v82, 0x1c000, v210
	ds_read_b128 v[42:45], v54
	ds_read_b128 v[46:49], v54 offset:1024
	ds_read_b128 v[50:53], v54 offset:2048
	ds_read_b128 v[54:57], v54 offset:3072
	ds_read_b128 v[162:165], v82
	ds_read_b128 v[174:177], v82 offset:1024
	ds_read_b128 v[186:189], v82 offset:2048
	ds_read_b128 v[190:193], v82 offset:3072
	s_mov_b32 s62, s85
	ds_read_b128 v[82:85], v209 offset:32768
	ds_read_b128 v[86:89], v209 offset:33792
	ds_read_b128 v[98:101], v209 offset:34816
	ds_read_b128 v[102:105], v209 offset:35840
	ds_read_b128 v[212:215], v209 offset:36864
	ds_read_b128 v[216:219], v209 offset:37888
	ds_read_b128 v[220:223], v209 offset:38912
	ds_read_b128 v[224:227], v209 offset:39936
	s_add_i32 s69, s69, 0x20000
	s_add_i32 m0, s62, 0x4000
	s_mov_b32 s62, s85
	buffer_load_dwordx4 v0, s[88:91], s69 offen lds
	s_add_i32 m0, s62, 0x6000
	s_nop 0
	buffer_load_dwordx4 v195, s[88:91], s69 offen lds
	s_cmp_lg_u32 s61, 0
	s_cbranch_scc1 .Lgr10
	s_waitcnt vmcnt(8)
; #define PG8_STAGE(bufoff, RS, soff, voff) do { _Pragma("unroll") for (int _i = 0; _i < 2; ++_i) \
;         __builtin_amdgcn_raw_ptr_buffer_load_lds(RS, (PG8_LAS void*)(lds + (bufoff) + sgpr_opaque(ldsw) + _i * 8192), 16, (int)(voff)[_i], (int)(soff), 0, 0); } while (0)
; #define PG8_LDA(dst, b, h) do { _Pragma("unroll") for (int m = 0; m < 4; ++m) _Pragma("unroll") for (int k = 0; k < 2; ++k) dst[m][k] = *(const PG8_LAS f16x8*)(lds + PG8_SA(b, h) + aoff + m * 2048 + k * 1024); } while (0)
; #define PG8_LDB(dst, b, h) do { _Pragma("unroll") for (int n = 0; n < 2; ++n) _Pragma("unroll") for (int k = 0; k < 2; ++k) dst[n][k] = *(const PG8_LAS f16x8*)(lds + PG8_SB(b, h) + boff + n * 2048 + k * 1024); } while (0)
; #define PG8_WAIT_L(n) asm volatile("s_waitcnt lgkmcnt(" #n ")" ::: "memory")
; #define PG8_BAR __builtin_amdgcn_s_barrier()
; #define PG8_SCHED __builtin_amdgcn_sched_barrier(0)
; template <class Epi, class Sched, bool ALIGN_EPI = false, bool SP2 = false, bool I8 = false, bool ATILED = false>
; __device__ __forceinline__ void gemm_phase(PG8_LAS unsigned char* lds, const Gemm g, const Sched& S, const Epi& E, const int wid) {
;     ...
;             PG8_LDB(B0, 0, 0); PG8_LDB(B1, 0, 1); PG8_SCHED; PG8_LDA(At, 0, 0); PG8_STAGE(PG8_SA(1, 1), rsA, a1 + hstepA, voffA);
;             PG8_WAIT_VG; PG8_WAIT_L(0); PG8_BAR; PG8_MMA(0, 0, At, B0); PG8_MMA(0, 1, At, B1); PG8_BAR; PG8_SCHED;
;             PG8_LDA(At, 0, 1); PG8_STAGE(PG8_SB(0, 0), rsB, b2, voffB); PG8_STAGE(PG8_SB(0, 1), rsB, b2 + hstep, voffB); PG8_STAGE(PG8_SA(0, 0), rsA, a2, voffA);
;             PG8_WAIT_VG; PG8_WAIT_L(0); PG8_BAR; PG8_MMA(1, 0, At, B0); PG8_MMA(1, 1, At, B1); PG8_BAR; PG8_SCHED;
;             PG8_LDB(B0, 1, 0); PG8_LDB(B1, 1, 1); PG8_SCHED; PG8_LDA(At, 1, 0); PG8_STAGE(PG8_SA(0, 1), rsA, a2 + hstepA, voffA);
;             PG8_WAIT_VG; PG8_WAIT_L(0); PG8_BAR; PG8_MMA(0, 0, At, B0); PG8_MMA(0, 1, At, B1); PG8_BAR; PG8_SCHED;
;             PG8_LDA(At, 1, 1); PG8_STAGE(PG8_SB(1, 0), rsB, b3, voffB); PG8_STAGE(PG8_SB(1, 1), rsB, b3 + hstep, voffB); PG8_STAGE(PG8_SA(1, 0), rsA, a3, voffA);
;             PG8_WAIT_VG; PG8_WAIT_L(0); PG8_BAR; PG8_MMA(1, 0, At, B0); PG8_MMA(1, 1, At, B1); PG8_BAR; PG8_SCHED;
.Lgr10:
	s_waitcnt vmcnt(36)
	s_waitcnt lgkmcnt(0)
	s_barrier
	s_setprio 0
	s_waitcnt lgkmcnt(7)
	v_mfma_i32_16x16x64_i8 v[134:137], v[42:45], v[82:85], v[182:185]
	s_waitcnt lgkmcnt(6)
	v_mfma_i32_16x16x64_i8 v[182:185], v[46:49], v[86:89], v[134:137]
	v_mfma_i32_16x16x64_i8 v[134:137], v[50:53], v[82:85], v[178:181]
	v_mfma_i32_16x16x64_i8 v[178:181], v[54:57], v[86:89], v[134:137]
	s_waitcnt lgkmcnt(5)
	v_mfma_i32_16x16x64_i8 v[134:137], v[42:45], v[98:101], v[158:161]
	s_waitcnt lgkmcnt(4)
	v_mfma_i32_16x16x64_i8 v[158:161], v[46:49], v[102:105], v[134:137]
	v_mfma_i32_16x16x64_i8 v[134:137], v[50:53], v[98:101], v[154:157]
	v_mfma_i32_16x16x64_i8 v[154:157], v[54:57], v[102:105], v[134:137]
	s_waitcnt lgkmcnt(3)
	v_mfma_i32_16x16x64_i8 v[134:137], v[42:45], v[212:215], v[142:145]
	s_waitcnt lgkmcnt(2)
	v_mfma_i32_16x16x64_i8 v[142:145], v[46:49], v[216:219], v[134:137]
	v_mfma_i32_16x16x64_i8 v[134:137], v[50:53], v[212:215], v[138:141]
	s_waitcnt lgkmcnt(1)
	v_mfma_i32_16x16x64_i8 v[126:129], v[42:45], v[220:223], v[126:129]
	v_mfma_i32_16x16x64_i8 v[122:125], v[50:53], v[220:223], v[122:125]
	v_mfma_i32_16x16x64_i8 v[138:141], v[54:57], v[216:219], v[134:137]
	s_waitcnt lgkmcnt(0)
	v_mfma_i32_16x16x64_i8 v[126:129], v[46:49], v[224:227], v[126:129]
	v_mfma_i32_16x16x64_i8 v[122:125], v[54:57], v[224:227], v[122:125]
	s_setprio 1
	s_setprio 0
	v_mfma_i32_16x16x64_i8 v[58:61], v[186:189], v[82:85], v[58:61]
	v_mfma_i32_16x16x64_i8 v[166:169], v[190:193], v[86:89], v[58:61]
	v_mfma_i32_16x16x64_i8 v[58:61], v[162:165], v[98:101], v[62:65]
	v_mfma_i32_16x16x64_i8 v[150:153], v[174:177], v[102:105], v[58:61]
	v_mfma_i32_16x16x64_i8 v[58:61], v[186:189], v[98:101], v[66:69]
	v_mfma_i32_16x16x64_i8 v[134:137], v[162:165], v[82:85], v[170:173]
	v_mfma_i32_16x16x64_i8 v[146:149], v[190:193], v[102:105], v[58:61]
	v_mfma_i32_16x16x64_i8 v[58:61], v[162:165], v[212:215], v[70:73]
	v_mfma_i32_16x16x64_i8 v[170:173], v[174:177], v[86:89], v[134:137]
	v_mfma_i32_16x16x64_i8 v[134:137], v[174:177], v[216:219], v[58:61]
	v_mfma_i32_16x16x64_i8 v[58:61], v[186:189], v[212:215], v[130:133]
	v_mfma_i32_16x16x64_i8 v[130:133], v[190:193], v[216:219], v[58:61]
	v_mfma_i32_16x16x64_i8 v[58:61], v[162:165], v[220:223], v[118:121]
	v_mfma_i32_16x16x64_i8 v[118:121], v[174:177], v[224:227], v[58:61]
	v_mfma_i32_16x16x64_i8 v[58:61], v[186:189], v[220:223], v[114:117]
	v_mfma_i32_16x16x64_i8 v[114:117], v[190:193], v[224:227], v[58:61]
	s_setprio 1
	s_barrier
	s_mov_b32 s62, s85
	s_nop 3
	ds_read_b128 v[58:61], v209 offset:49152
	ds_read_b128 v[62:65], v209 offset:50176
	ds_read_b128 v[66:69], v209 offset:51200
	ds_read_b128 v[70:73], v209 offset:52224
	ds_read_b128 v[212:215], v209 offset:53248
	ds_read_b128 v[216:219], v209 offset:54272
	ds_read_b128 v[220:223], v209 offset:55296
	ds_read_b128 v[224:227], v209 offset:56320
	s_add_i32 m0, s62, 0x18000
	s_mov_b32 s62, s85
	buffer_load_dwordx4 v194, s[64:67], s53 offen lds
	s_add_i32 m0, s62, 0x1a000
	s_add_i32 s52, s52, 0xc000
	buffer_load_dwordx4 v196, s[64:67], s53 offen lds
	s_mov_b32 s53, s85
	s_add_i32 m0, s53, 0x1c000
	s_mov_b32 s53, s85
	buffer_load_dwordx4 v194, s[64:67], s52 offen lds
	s_add_i32 m0, s53, 0x1e000
	s_nop 0
	buffer_load_dwordx4 v196, s[64:67], s52 offen lds
	s_mov_b32 s52, s85
	s_add_i32 m0, s52, 0x8000
	s_mov_b32 s52, s85
	buffer_load_dwordx4 v0, s[88:91], s51 offen lds
	s_add_i32 m0, s52, 0xa000
	s_nop 0
	buffer_load_dwordx4 v195, s[88:91], s51 offen lds
	s_cmp_lg_u32 s61, 0
	s_cbranch_scc1 .Lgr11
	s_waitcnt vmcnt(8)
.Lgr11:
	s_waitcnt vmcnt(36)
	s_waitcnt lgkmcnt(0)
	s_barrier
	s_setprio 0
	s_waitcnt lgkmcnt(7)
	v_mfma_i32_16x16x64_i8 v[82:85], v[42:45], v[58:61], v[110:113]
	s_waitcnt lgkmcnt(6)
	v_mfma_i32_16x16x64_i8 v[110:113], v[46:49], v[62:65], v[82:85]
	v_mfma_i32_16x16x64_i8 v[82:85], v[50:53], v[58:61], v[106:109]
	v_mfma_i32_16x16x64_i8 v[106:109], v[54:57], v[62:65], v[82:85]
	s_waitcnt lgkmcnt(5)
	v_mfma_i32_16x16x64_i8 v[82:85], v[42:45], v[66:69], v[94:97]
	s_waitcnt lgkmcnt(4)
	v_mfma_i32_16x16x64_i8 v[94:97], v[46:49], v[70:73], v[82:85]
	v_mfma_i32_16x16x64_i8 v[82:85], v[50:53], v[66:69], v[90:93]
	s_waitcnt lgkmcnt(3)
	v_mfma_i32_16x16x64_i8 v[78:81], v[42:45], v[212:215], v[78:81]
	v_mfma_i32_16x16x64_i8 v[74:77], v[50:53], v[212:215], v[74:77]
	s_waitcnt lgkmcnt(1)
	v_mfma_i32_16x16x64_i8 v[14:17], v[42:45], v[220:223], v[14:17]
	v_mfma_i32_16x16x64_i8 v[10:13], v[50:53], v[220:223], v[10:13]
	v_mfma_i32_16x16x64_i8 v[90:93], v[54:57], v[70:73], v[82:85]
	v_mfma_i32_16x16x64_i8 v[78:81], v[46:49], v[216:219], v[78:81]
	v_mfma_i32_16x16x64_i8 v[74:77], v[54:57], v[216:219], v[74:77]
	s_waitcnt lgkmcnt(0)
	v_mfma_i32_16x16x64_i8 v[14:17], v[46:49], v[224:227], v[14:17]
	v_mfma_i32_16x16x64_i8 v[10:13], v[54:57], v[224:227], v[10:13]
	s_setprio 1
	s_setprio 0
	v_mfma_i32_16x16x64_i8 v[26:29], v[162:165], v[58:61], v[26:29]
	v_mfma_i32_16x16x64_i8 v[102:105], v[174:177], v[62:65], v[26:29]
	v_mfma_i32_16x16x64_i8 v[26:29], v[186:189], v[58:61], v[30:33]
	v_mfma_i32_16x16x64_i8 v[98:101], v[190:193], v[62:65], v[26:29]
	v_mfma_i32_16x16x64_i8 v[26:29], v[162:165], v[66:69], v[34:37]
	v_mfma_i32_16x16x64_i8 v[86:89], v[174:177], v[70:73], v[26:29]
	v_mfma_i32_16x16x64_i8 v[26:29], v[186:189], v[66:69], v[38:41]
	v_mfma_i32_16x16x64_i8 v[22:25], v[162:165], v[212:215], v[22:25]
	v_mfma_i32_16x16x64_i8 v[18:21], v[186:189], v[212:215], v[18:21]
	v_mfma_i32_16x16x64_i8 v[6:9], v[162:165], v[220:223], v[6:9]
	v_mfma_i32_16x16x64_i8 v[2:5], v[186:189], v[220:223], v[2:5]
	v_mfma_i32_16x16x64_i8 v[82:85], v[190:193], v[70:73], v[26:29]
	v_mfma_i32_16x16x64_i8 v[22:25], v[174:177], v[216:219], v[22:25]
	v_mfma_i32_16x16x64_i8 v[18:21], v[190:193], v[216:219], v[18:21]
	v_mfma_i32_16x16x64_i8 v[6:9], v[174:177], v[224:227], v[6:9]
	v_mfma_i32_16x16x64_i8 v[2:5], v[190:193], v[224:227], v[2:5]
	s_setprio 1
	s_barrier
	s_add_i32 s50, s50, 2
	s_addk_i32 s48, 0x100
	s_add_i32 s49, s49, 0x10000
	s_cmp_gt_u32 s50, 5
	s_cbranch_scc0 .LBB0_1223
	s_and_b64 vcc, exec, s[56:57]
	s_cbranch_vccz .LBB0_1226
	s_barrier

; #define PG8_STAGE(bufoff, RS, soff, voff) do { _Pragma("unroll") for (int _i = 0; _i < 2; ++_i) \
;         __builtin_amdgcn_raw_ptr_buffer_load_lds(RS, (PG8_LAS void*)(lds + (bufoff) + sgpr_opaque(ldsw) + _i * 8192), 16, (int)(voff)[_i], (int)(soff), 0, 0); } while (0)
; #define PG8_LDA(dst, b, h) do { _Pragma("unroll") for (int m = 0; m < 4; ++m) _Pragma("unroll") for (int k = 0; k < 2; ++k) dst[m][k] = *(const PG8_LAS f16x8*)(lds + PG8_SA(b, h) + aoff + m * 2048 + k * 1024); } while (0)
; #define PG8_LDB(dst, b, h) do { _Pragma("unroll") for (int n = 0; n < 2; ++n) _Pragma("unroll") for (int k = 0; k < 2; ++k) dst[n][k] = *(const PG8_LAS f16x8*)(lds + PG8_SB(b, h) + boff + n * 2048 + k * 1024); } while (0)
; #define PG8_WAIT_L(n) asm volatile("s_waitcnt lgkmcnt(" #n ")" ::: "memory")
; #define PG8_BAR __builtin_amdgcn_s_barrier()
; #define PG8_SCHED __builtin_amdgcn_sched_barrier(0)
; template <class Epi, class Sched, bool ALIGN_EPI = false, bool SP2 = false, bool I8 = false, bool ATILED = false>
; __device__ __forceinline__ void gemm_phase(PG8_LAS unsigned char* lds, const Gemm g, const Sched& S, const Epi& E, const int wid) {
;     ...
;             PG8_LDB(B0, 0, 0); PG8_LDB(B1, 0, 1); PG8_SCHED; PG8_LDA(At, 0, 0); PG8_STAGE(PG8_SA(1, 1), rsA, a1 + hstepA, voffA);
;             PG8_WAIT_VG; PG8_WAIT_L(0); PG8_BAR; PG8_MMA(0, 0, At, B0); PG8_MMA(0, 1, At, B1); PG8_BAR; PG8_SCHED;
;             PG8_LDA(At, 0, 1); PG8_STAGE(PG8_SB(0, 0), rsB, b2, voffB); PG8_STAGE(PG8_SB(0, 1), rsB, b2 + hstep, voffB); PG8_STAGE(PG8_SA(0, 0), rsA, a2, voffA);
;             PG8_WAIT_VG; PG8_WAIT_L(0); PG8_BAR; PG8_MMA(1, 0, At, B0); PG8_MMA(1, 1, At, B1); PG8_BAR; PG8_SCHED;
;             PG8_LDB(B0, 1, 0); PG8_LDB(B1, 1, 1); PG8_SCHED; PG8_LDA(At, 1, 0); PG8_STAGE(PG8_SA(0, 1), rsA, a2 + hstepA, voffA);
;             PG8_WAIT_VG; PG8_WAIT_L(0); PG8_BAR; PG8_MMA(0, 0, At, B0); PG8_MMA(0, 1, At, B1); PG8_BAR; PG8_SCHED;
;             PG8_LDA(At, 1, 1); PG8_STAGE(PG8_SB(1, 0), rsB, b3, voffB); PG8_STAGE(PG8_SB(1, 1), rsB, b3 + hstep, voffB); PG8_STAGE(PG8_SA(1, 0), rsA, a3, voffA);
;             PG8_WAIT_VG; PG8_WAIT_L(0); PG8_BAR; PG8_MMA(1, 0, At, B0); PG8_MMA(1, 1, At, B1); PG8_BAR; PG8_SCHED;
.Lgr12:
	s_waitcnt vmcnt(40)
	s_waitcnt lgkmcnt(0)
	s_barrier
	s_setprio 0
	s_waitcnt lgkmcnt(7)
	v_mfma_f32_16x16x32_f16 v[142:145], v[66:69], v[162:165], v[142:145]
	v_mfma_f32_16x16x32_f16 v[138:141], v[74:77], v[162:165], v[138:141]
	s_waitcnt lgkmcnt(5)
	v_mfma_f32_16x16x32_f16 v[126:129], v[66:69], v[170:173], v[126:129]
	v_mfma_f32_16x16x32_f16 v[122:125], v[74:77], v[170:173], v[122:125]
	s_waitcnt lgkmcnt(3)
	v_mfma_f32_16x16x32_f16 v[114:117], v[66:69], v[178:181], v[114:117]
	v_mfma_f32_16x16x32_f16 v[106:109], v[74:77], v[178:181], v[106:109]
	s_waitcnt lgkmcnt(1)
	v_mfma_f32_16x16x32_f16 v[102:105], v[66:69], v[194:197], v[102:105]
	v_mfma_f32_16x16x32_f16 v[94:97], v[74:77], v[194:197], v[94:97]
	v_mfma_f32_16x16x32_f16 v[142:145], v[70:73], v[166:169], v[142:145]
	v_mfma_f32_16x16x32_f16 v[138:141], v[78:81], v[166:169], v[138:141]
	v_mfma_f32_16x16x32_f16 v[126:129], v[70:73], v[174:177], v[126:129]
	v_mfma_f32_16x16x32_f16 v[122:125], v[78:81], v[174:177], v[122:125]
	v_mfma_f32_16x16x32_f16 v[114:117], v[70:73], v[182:185], v[114:117]
	v_mfma_f32_16x16x32_f16 v[106:109], v[78:81], v[182:185], v[106:109]
	s_waitcnt lgkmcnt(0)
	v_mfma_f32_16x16x32_f16 v[102:105], v[70:73], v[208:211], v[102:105]
	v_mfma_f32_16x16x32_f16 v[94:97], v[78:81], v[208:211], v[94:97]
	s_setprio 1
	s_setprio 0
	v_mfma_f32_16x16x32_f16 v[134:137], v[146:149], v[162:165], v[134:137]
	v_mfma_f32_16x16x32_f16 v[130:133], v[154:157], v[162:165], v[130:133]
	v_mfma_f32_16x16x32_f16 v[118:121], v[146:149], v[170:173], v[118:121]
	v_mfma_f32_16x16x32_f16 v[110:113], v[154:157], v[170:173], v[110:113]
	v_mfma_f32_16x16x32_f16 v[98:101], v[146:149], v[178:181], v[98:101]
	v_mfma_f32_16x16x32_f16 v[90:93], v[154:157], v[178:181], v[90:93]
	v_mfma_f32_16x16x32_f16 v[86:89], v[146:149], v[194:197], v[86:89]
	v_mfma_f32_16x16x32_f16 v[82:85], v[154:157], v[194:197], v[82:85]
	v_mfma_f32_16x16x32_f16 v[134:137], v[150:153], v[166:169], v[134:137]
	v_mfma_f32_16x16x32_f16 v[130:133], v[158:161], v[166:169], v[130:133]
	v_mfma_f32_16x16x32_f16 v[118:121], v[150:153], v[174:177], v[118:121]
	v_mfma_f32_16x16x32_f16 v[110:113], v[158:161], v[174:177], v[110:113]
	v_mfma_f32_16x16x32_f16 v[98:101], v[150:153], v[182:185], v[98:101]
	v_mfma_f32_16x16x32_f16 v[90:93], v[158:161], v[182:185], v[90:93]
	v_mfma_f32_16x16x32_f16 v[86:89], v[150:153], v[208:211], v[86:89]
	v_mfma_f32_16x16x32_f16 v[82:85], v[158:161], v[208:211], v[82:85]
	s_setprio 1
	s_barrier
	s_mov_b32 s38, s85
	ds_read_b128 v[162:165], v190 offset:16384
	ds_read_b128 v[166:169], v190 offset:17408
	ds_read_b128 v[170:173], v190 offset:18432
	ds_read_b128 v[174:177], v190 offset:19456
	ds_read_b128 v[178:181], v190 offset:20480
	ds_read_b128 v[182:185], v190 offset:21504
	ds_read_b128 v[194:197], v190 offset:22528
	ds_read_b128 v[208:211], v190 offset:23552
	s_add_i32 m0, s38, 0x10000
	s_mov_b32 s38, s66
	s_mov_b32 s39, s67
	s_mov_b32 s61, s85
	buffer_load_dwordx4 v186, s[36:39], s55 offen lds
	s_add_i32 m0, s61, 0x12000
	s_mov_b32 s62, s85
	buffer_load_dwordx4 v188, s[36:39], s55 offen lds
	s_add_i32 s61, s55, 0x40000
	s_add_i32 m0, s62, 0x14000
	s_mov_b32 s62, s85
	buffer_load_dwordx4 v186, s[36:39], s61 offen lds
	s_add_i32 m0, s62, 0x16000
	s_nop 0
	buffer_load_dwordx4 v188, s[36:39], s61 offen lds
	s_mov_b32 s61, s85
	s_mov_b32 m0, s61
	s_mov_b32 s61, s85
	buffer_load_dwordx4 v0, s[64:67], s60 offen lds
	s_add_i32 m0, s61, 0x2000
	s_nop 0
	buffer_load_dwordx4 v187, s[64:67], s60 offen lds
	s_cmp_lg_u32 s59, 0
	s_cbranch_scc1 .Lgr13
	s_waitcnt vmcnt(8)
.Lgr13:
	s_waitcnt vmcnt(40)
	s_waitcnt lgkmcnt(0)
	s_barrier
	s_setprio 0
	s_waitcnt lgkmcnt(7)
	v_mfma_f32_16x16x32_f16 v[62:65], v[66:69], v[162:165], v[62:65]
	v_mfma_f32_16x16x32_f16 v[58:61], v[74:77], v[162:165], v[58:61]
	s_waitcnt lgkmcnt(5)
	v_mfma_f32_16x16x32_f16 v[50:53], v[66:69], v[170:173], v[50:53]
	v_mfma_f32_16x16x32_f16 v[42:45], v[74:77], v[170:173], v[42:45]
	s_waitcnt lgkmcnt(3)
	v_mfma_f32_16x16x32_f16 v[34:37], v[66:69], v[178:181], v[34:37]
	v_mfma_f32_16x16x32_f16 v[26:29], v[74:77], v[178:181], v[26:29]
	s_waitcnt lgkmcnt(1)
	v_mfma_f32_16x16x32_f16 v[18:21], v[66:69], v[194:197], v[18:21]
	v_mfma_f32_16x16x32_f16 v[10:13], v[74:77], v[194:197], v[10:13]
	v_mfma_f32_16x16x32_f16 v[62:65], v[70:73], v[166:169], v[62:65]
	v_mfma_f32_16x16x32_f16 v[58:61], v[78:81], v[166:169], v[58:61]
	v_mfma_f32_16x16x32_f16 v[50:53], v[70:73], v[174:177], v[50:53]
	v_mfma_f32_16x16x32_f16 v[42:45], v[78:81], v[174:177], v[42:45]
	v_mfma_f32_16x16x32_f16 v[34:37], v[70:73], v[182:185], v[34:37]
	v_mfma_f32_16x16x32_f16 v[26:29], v[78:81], v[182:185], v[26:29]
	s_waitcnt lgkmcnt(0)
	v_mfma_f32_16x16x32_f16 v[18:21], v[70:73], v[208:211], v[18:21]
	v_mfma_f32_16x16x32_f16 v[10:13], v[78:81], v[208:211], v[10:13]
	s_setprio 1
	s_setprio 0
	v_mfma_f32_16x16x32_f16 v[54:57], v[146:149], v[162:165], v[54:57]
	v_mfma_f32_16x16x32_f16 v[46:49], v[154:157], v[162:165], v[46:49]
	v_mfma_f32_16x16x32_f16 v[38:41], v[146:149], v[170:173], v[38:41]
	v_mfma_f32_16x16x32_f16 v[30:33], v[154:157], v[170:173], v[30:33]
	v_mfma_f32_16x16x32_f16 v[22:25], v[146:149], v[178:181], v[22:25]
	v_mfma_f32_16x16x32_f16 v[14:17], v[154:157], v[178:181], v[14:17]
	v_mfma_f32_16x16x32_f16 v[6:9], v[146:149], v[194:197], v[6:9]
	v_mfma_f32_16x16x32_f16 v[2:5], v[154:157], v[194:197], v[2:5]
	v_mfma_f32_16x16x32_f16 v[54:57], v[150:153], v[166:169], v[54:57]
	v_mfma_f32_16x16x32_f16 v[46:49], v[158:161], v[166:169], v[46:49]
	v_mfma_f32_16x16x32_f16 v[38:41], v[150:153], v[174:177], v[38:41]
	v_mfma_f32_16x16x32_f16 v[30:33], v[158:161], v[174:177], v[30:33]
	v_mfma_f32_16x16x32_f16 v[22:25], v[150:153], v[182:185], v[22:25]
	v_mfma_f32_16x16x32_f16 v[14:17], v[158:161], v[182:185], v[14:17]
	v_mfma_f32_16x16x32_f16 v[6:9], v[150:153], v[208:211], v[6:9]
	v_mfma_f32_16x16x32_f16 v[2:5], v[158:161], v[208:211], v[2:5]
	s_setprio 1
	s_barrier
	v_add_u32_e32 v78, 0x18000, v191
	v_add_u32_e32 v158, 0x1c000, v191
	ds_read_b128 v[66:69], v78
	ds_read_b128 v[70:73], v78 offset:1024
	ds_read_b128 v[74:77], v78 offset:2048
	ds_read_b128 v[78:81], v78 offset:3072
	ds_read_b128 v[146:149], v158
	ds_read_b128 v[150:153], v158 offset:1024
	ds_read_b128 v[154:157], v158 offset:2048
	ds_read_b128 v[158:161], v158 offset:3072
	s_mov_b32 s61, s85
	ds_read_b128 v[162:165], v190 offset:32768
	ds_read_b128 v[166:169], v190 offset:33792
	ds_read_b128 v[170:173], v190 offset:34816
	ds_read_b128 v[174:177], v190 offset:35840
	ds_read_b128 v[178:181], v190 offset:36864
	ds_read_b128 v[182:185], v190 offset:37888
	ds_read_b128 v[194:197], v190 offset:38912
	ds_read_b128 v[208:211], v190 offset:39936
	s_add_i32 s60, s60, 0x40000
	s_add_i32 m0, s61, 0x4000
	s_mov_b32 s61, s85
	buffer_load_dwordx4 v0, s[64:67], s60 offen lds
	s_add_i32 m0, s61, 0x6000
	s_nop 0
	buffer_load_dwordx4 v187, s[64:67], s60 offen lds
	s_cmp_lg_u32 s59, 0
	s_cbranch_scc1 .Lgr14
	s_waitcnt vmcnt(8)
; #define PG8_STAGE(bufoff, RS, soff, voff) do { _Pragma("unroll") for (int _i = 0; _i < 2; ++_i) \
;         __builtin_amdgcn_raw_ptr_buffer_load_lds(RS, (PG8_LAS void*)(lds + (bufoff) + sgpr_opaque(ldsw) + _i * 8192), 16, (int)(voff)[_i], (int)(soff), 0, 0); } while (0)
; #define PG8_LDA(dst, b, h) do { _Pragma("unroll") for (int m = 0; m < 4; ++m) _Pragma("unroll") for (int k = 0; k < 2; ++k) dst[m][k] = *(const PG8_LAS f16x8*)(lds + PG8_SA(b, h) + aoff + m * 2048 + k * 1024); } while (0)
; #define PG8_LDB(dst, b, h) do { _Pragma("unroll") for (int n = 0; n < 2; ++n) _Pragma("unroll") for (int k = 0; k < 2; ++k) dst[n][k] = *(const PG8_LAS f16x8*)(lds + PG8_SB(b, h) + boff + n * 2048 + k * 1024); } while (0)
; #define PG8_WAIT_L(n) asm volatile("s_waitcnt lgkmcnt(" #n ")" ::: "memory")
; #define PG8_BAR __builtin_amdgcn_s_barrier()
; #define PG8_SCHED __builtin_amdgcn_sched_barrier(0)
; template <class Epi, class Sched, bool ALIGN_EPI = false, bool SP2 = false, bool I8 = false, bool ATILED = false>
; __device__ __forceinline__ void gemm_phase(PG8_LAS unsigned char* lds, const Gemm g, const Sched& S, const Epi& E, const int wid) {
;     ...
;             PG8_LDB(B0, 0, 0); PG8_LDB(B1, 0, 1); PG8_SCHED; PG8_LDA(At, 0, 0); PG8_STAGE(PG8_SA(1, 1), rsA, a1 + hstepA, voffA);
;             PG8_WAIT_VG; PG8_WAIT_L(0); PG8_BAR; PG8_MMA(0, 0, At, B0); PG8_MMA(0, 1, At, B1); PG8_BAR; PG8_SCHED;
;             PG8_LDA(At, 0, 1); PG8_STAGE(PG8_SB(0, 0), rsB, b2, voffB); PG8_STAGE(PG8_SB(0, 1), rsB, b2 + hstep, voffB); PG8_STAGE(PG8_SA(0, 0), rsA, a2, voffA);
;             PG8_WAIT_VG; PG8_WAIT_L(0); PG8_BAR; PG8_MMA(1, 0, At, B0); PG8_MMA(1, 1, At, B1); PG8_BAR; PG8_SCHED;
;             PG8_LDB(B0, 1, 0); PG8_LDB(B1, 1, 1); PG8_SCHED; PG8_LDA(At, 1, 0); PG8_STAGE(PG8_SA(0, 1), rsA, a2 + hstepA, voffA);
;             PG8_WAIT_VG; PG8_WAIT_L(0); PG8_BAR; PG8_MMA(0, 0, At, B0); PG8_MMA(0, 1, At, B1); PG8_BAR; PG8_SCHED;
;             PG8_LDA(At, 1, 1); PG8_STAGE(PG8_SB(1, 0), rsB, b3, voffB); PG8_STAGE(PG8_SB(1, 1), rsB, b3 + hstep, voffB); PG8_STAGE(PG8_SA(1, 0), rsA, a3, voffA);
;             PG8_WAIT_VG; PG8_WAIT_L(0); PG8_BAR; PG8_MMA(1, 0, At, B0); PG8_MMA(1, 1, At, B1); PG8_BAR; PG8_SCHED;
.Lgr14:
	s_waitcnt vmcnt(40)
	s_waitcnt lgkmcnt(0)
	s_barrier
	s_setprio 0
	s_waitcnt lgkmcnt(7)
	v_mfma_f32_16x16x32_f16 v[142:145], v[66:69], v[162:165], v[142:145]
	v_mfma_f32_16x16x32_f16 v[138:141], v[74:77], v[162:165], v[138:141]
	s_waitcnt lgkmcnt(5)
	v_mfma_f32_16x16x32_f16 v[126:129], v[66:69], v[170:173], v[126:129]
	v_mfma_f32_16x16x32_f16 v[122:125], v[74:77], v[170:173], v[122:125]
	s_waitcnt lgkmcnt(3)
	v_mfma_f32_16x16x32_f16 v[114:117], v[66:69], v[178:181], v[114:117]
	v_mfma_f32_16x16x32_f16 v[106:109], v[74:77], v[178:181], v[106:109]
	s_waitcnt lgkmcnt(1)
	v_mfma_f32_16x16x32_f16 v[102:105], v[66:69], v[194:197], v[102:105]
	v_mfma_f32_16x16x32_f16 v[94:97], v[74:77], v[194:197], v[94:97]
	v_mfma_f32_16x16x32_f16 v[142:145], v[70:73], v[166:169], v[142:145]
	v_mfma_f32_16x16x32_f16 v[138:141], v[78:81], v[166:169], v[138:141]
	v_mfma_f32_16x16x32_f16 v[126:129], v[70:73], v[174:177], v[126:129]
	v_mfma_f32_16x16x32_f16 v[122:125], v[78:81], v[174:177], v[122:125]
	v_mfma_f32_16x16x32_f16 v[114:117], v[70:73], v[182:185], v[114:117]
	v_mfma_f32_16x16x32_f16 v[106:109], v[78:81], v[182:185], v[106:109]
	s_waitcnt lgkmcnt(0)
	v_mfma_f32_16x16x32_f16 v[102:105], v[70:73], v[208:211], v[102:105]
	v_mfma_f32_16x16x32_f16 v[94:97], v[78:81], v[208:211], v[94:97]
	s_setprio 1
	s_setprio 0
	v_mfma_f32_16x16x32_f16 v[134:137], v[146:149], v[162:165], v[134:137]
	v_mfma_f32_16x16x32_f16 v[130:133], v[154:157], v[162:165], v[130:133]
	v_mfma_f32_16x16x32_f16 v[118:121], v[146:149], v[170:173], v[118:121]
	v_mfma_f32_16x16x32_f16 v[110:113], v[154:157], v[170:173], v[110:113]
	v_mfma_f32_16x16x32_f16 v[98:101], v[146:149], v[178:181], v[98:101]
	v_mfma_f32_16x16x32_f16 v[90:93], v[154:157], v[178:181], v[90:93]
	v_mfma_f32_16x16x32_f16 v[86:89], v[146:149], v[194:197], v[86:89]
	v_mfma_f32_16x16x32_f16 v[82:85], v[154:157], v[194:197], v[82:85]
	v_mfma_f32_16x16x32_f16 v[134:137], v[150:153], v[166:169], v[134:137]
	v_mfma_f32_16x16x32_f16 v[130:133], v[158:161], v[166:169], v[130:133]
	v_mfma_f32_16x16x32_f16 v[118:121], v[150:153], v[174:177], v[118:121]
	v_mfma_f32_16x16x32_f16 v[110:113], v[158:161], v[174:177], v[110:113]
	v_mfma_f32_16x16x32_f16 v[98:101], v[150:153], v[182:185], v[98:101]
	v_mfma_f32_16x16x32_f16 v[90:93], v[158:161], v[182:185], v[90:93]
	v_mfma_f32_16x16x32_f16 v[86:89], v[150:153], v[208:211], v[86:89]
	v_mfma_f32_16x16x32_f16 v[82:85], v[158:161], v[208:211], v[82:85]
	s_setprio 1
	s_barrier
	s_mov_b32 s60, s85
	ds_read_b128 v[162:165], v190 offset:49152
	ds_read_b128 v[166:169], v190 offset:50176
	ds_read_b128 v[170:173], v190 offset:51200
	ds_read_b128 v[174:177], v190 offset:52224
	ds_read_b128 v[178:181], v190 offset:53248
	ds_read_b128 v[182:185], v190 offset:54272
	ds_read_b128 v[194:197], v190 offset:55296
	ds_read_b128 v[208:211], v190 offset:56320
	s_add_i32 m0, s60, 0x18000
	s_mov_b32 s60, s85
	buffer_load_dwordx4 v186, s[36:39], s58 offen lds
	s_add_i32 m0, s60, 0x1a000
	s_add_i32 s55, s55, 0x40080
	buffer_load_dwordx4 v188, s[36:39], s58 offen lds
	s_mov_b32 s58, s85
	s_add_i32 m0, s58, 0x1c000
	s_mov_b32 s58, s85
	buffer_load_dwordx4 v186, s[36:39], s55 offen lds
	s_add_i32 m0, s58, 0x1e000
	s_nop 0
	buffer_load_dwordx4 v188, s[36:39], s55 offen lds
	s_mov_b32 s38, s85
	s_add_i32 m0, s38, 0x8000
	s_mov_b32 s38, s85
	buffer_load_dwordx4 v0, s[64:67], s54 offen lds
	s_add_i32 m0, s38, 0xa000
	s_nop 0
	buffer_load_dwordx4 v187, s[64:67], s54 offen lds
	s_cmp_lg_u32 s59, 0
	s_cbranch_scc1 .Lgr15
	s_waitcnt vmcnt(8)
.Lgr15:
	s_waitcnt vmcnt(40)
	s_waitcnt lgkmcnt(0)
	s_barrier
	s_setprio 0
	s_waitcnt lgkmcnt(7)
	v_mfma_f32_16x16x32_f16 v[62:65], v[66:69], v[162:165], v[62:65]
	v_mfma_f32_16x16x32_f16 v[58:61], v[74:77], v[162:165], v[58:61]
	s_waitcnt lgkmcnt(5)
	v_mfma_f32_16x16x32_f16 v[50:53], v[66:69], v[170:173], v[50:53]
	v_mfma_f32_16x16x32_f16 v[42:45], v[74:77], v[170:173], v[42:45]
	s_waitcnt lgkmcnt(3)
	v_mfma_f32_16x16x32_f16 v[34:37], v[66:69], v[178:181], v[34:37]
	v_mfma_f32_16x16x32_f16 v[26:29], v[74:77], v[178:181], v[26:29]
	s_waitcnt lgkmcnt(1)
	v_mfma_f32_16x16x32_f16 v[18:21], v[66:69], v[194:197], v[18:21]
	v_mfma_f32_16x16x32_f16 v[10:13], v[74:77], v[194:197], v[10:13]
	v_mfma_f32_16x16x32_f16 v[62:65], v[70:73], v[166:169], v[62:65]
	v_mfma_f32_16x16x32_f16 v[58:61], v[78:81], v[166:169], v[58:61]
	v_mfma_f32_16x16x32_f16 v[50:53], v[70:73], v[174:177], v[50:53]
	v_mfma_f32_16x16x32_f16 v[42:45], v[78:81], v[174:177], v[42:45]
	v_mfma_f32_16x16x32_f16 v[34:37], v[70:73], v[182:185], v[34:37]
	v_mfma_f32_16x16x32_f16 v[26:29], v[78:81], v[182:185], v[26:29]
	s_waitcnt lgkmcnt(0)
	v_mfma_f32_16x16x32_f16 v[18:21], v[70:73], v[208:211], v[18:21]
	v_mfma_f32_16x16x32_f16 v[10:13], v[78:81], v[208:211], v[10:13]
	s_setprio 1
	s_setprio 0
	v_mfma_f32_16x16x32_f16 v[54:57], v[146:149], v[162:165], v[54:57]
	v_mfma_f32_16x16x32_f16 v[46:49], v[154:157], v[162:165], v[46:49]
	v_mfma_f32_16x16x32_f16 v[38:41], v[146:149], v[170:173], v[38:41]
	v_mfma_f32_16x16x32_f16 v[30:33], v[154:157], v[170:173], v[30:33]
	v_mfma_f32_16x16x32_f16 v[22:25], v[146:149], v[178:181], v[22:25]
	v_mfma_f32_16x16x32_f16 v[14:17], v[154:157], v[178:181], v[14:17]
	v_mfma_f32_16x16x32_f16 v[6:9], v[146:149], v[194:197], v[6:9]
	v_mfma_f32_16x16x32_f16 v[2:5], v[154:157], v[194:197], v[2:5]
	v_mfma_f32_16x16x32_f16 v[54:57], v[150:153], v[166:169], v[54:57]
	v_mfma_f32_16x16x32_f16 v[46:49], v[158:161], v[166:169], v[46:49]
	v_mfma_f32_16x16x32_f16 v[38:41], v[150:153], v[174:177], v[38:41]
	v_mfma_f32_16x16x32_f16 v[30:33], v[158:161], v[174:177], v[30:33]
	v_mfma_f32_16x16x32_f16 v[22:25], v[150:153], v[182:185], v[22:25]
	v_mfma_f32_16x16x32_f16 v[14:17], v[158:161], v[182:185], v[14:17]
	v_mfma_f32_16x16x32_f16 v[6:9], v[150:153], v[208:211], v[6:9]
	v_mfma_f32_16x16x32_f16 v[2:5], v[158:161], v[208:211], v[2:5]
	s_setprio 1
	s_barrier
	s_add_i32 s53, s53, 2
	s_addk_i32 s51, 0x100
	s_addk_i32 s52, 0x100
	s_cmp_gt_u32 s53, 13
	s_cbranch_scc0 .LBB0_1378
	s_and_b64 vcc, exec, s[56:57]
	s_cbranch_vccz .LBB0_1381
	s_barrier

; #define PG8_STAGE(bufoff, RS, soff, voff) do { _Pragma("unroll") for (int _i = 0; _i < 2; ++_i) \
;         __builtin_amdgcn_raw_ptr_buffer_load_lds(RS, (PG8_LAS void*)(lds + (bufoff) + sgpr_opaque(ldsw) + _i * 8192), 16, (int)(voff)[_i], (int)(soff), 0, 0); } while (0)
; #define PG8_LDA(dst, b, h) do { _Pragma("unroll") for (int m = 0; m < 4; ++m) _Pragma("unroll") for (int k = 0; k < 2; ++k) dst[m][k] = *(const PG8_LAS f16x8*)(lds + PG8_SA(b, h) + aoff + m * 2048 + k * 1024); } while (0)
; #define PG8_LDB(dst, b, h) do { _Pragma("unroll") for (int n = 0; n < 2; ++n) _Pragma("unroll") for (int k = 0; k < 2; ++k) dst[n][k] = *(const PG8_LAS f16x8*)(lds + PG8_SB(b, h) + boff + n * 2048 + k * 1024); } while (0)
; #define PG8_WAIT_L(n) asm volatile("s_waitcnt lgkmcnt(" #n ")" ::: "memory")
; #define PG8_BAR __builtin_amdgcn_s_barrier()
; #define PG8_SCHED __builtin_amdgcn_sched_barrier(0)
; template <class Epi, class Sched, bool ALIGN_EPI = false, bool SP2 = false, bool I8 = false, bool ATILED = false>
; __device__ __forceinline__ void gemm_phase(PG8_LAS unsigned char* lds, const Gemm g, const Sched& S, const Epi& E, const int wid) {
;     ...
;             PG8_LDB(B0, 0, 0); PG8_LDB(B1, 0, 1); PG8_SCHED; PG8_LDA(At, 0, 0); PG8_STAGE(PG8_SA(1, 1), rsA, a1 + hstepA, voffA);
;             PG8_WAIT_VG; PG8_WAIT_L(0); PG8_BAR; PG8_MMA(0, 0, At, B0); PG8_MMA(0, 1, At, B1); PG8_BAR; PG8_SCHED;
;             PG8_LDA(At, 0, 1); PG8_STAGE(PG8_SB(0, 0), rsB, b2, voffB); PG8_STAGE(PG8_SB(0, 1), rsB, b2 + hstep, voffB); PG8_STAGE(PG8_SA(0, 0), rsA, a2, voffA);
;             PG8_WAIT_VG; PG8_WAIT_L(0); PG8_BAR; PG8_MMA(1, 0, At, B0); PG8_MMA(1, 1, At, B1); PG8_BAR; PG8_SCHED;
;             PG8_LDB(B0, 1, 0); PG8_LDB(B1, 1, 1); PG8_SCHED; PG8_LDA(At, 1, 0); PG8_STAGE(PG8_SA(0, 1), rsA, a2 + hstepA, voffA);
;             PG8_WAIT_VG; PG8_WAIT_L(0); PG8_BAR; PG8_MMA(0, 0, At, B0); PG8_MMA(0, 1, At, B1); PG8_BAR; PG8_SCHED;
;             PG8_LDA(At, 1, 1); PG8_STAGE(PG8_SB(1, 0), rsB, b3, voffB); PG8_STAGE(PG8_SB(1, 1), rsB, b3 + hstep, voffB); PG8_STAGE(PG8_SA(1, 0), rsA, a3, voffA);
;             PG8_WAIT_VG; PG8_WAIT_L(0); PG8_BAR; PG8_MMA(1, 0, At, B0); PG8_MMA(1, 1, At, B1); PG8_BAR; PG8_SCHED;
.Lgr16:
	s_waitcnt vmcnt(24)
	s_waitcnt lgkmcnt(0)
	s_barrier
	s_setprio 0
	s_waitcnt lgkmcnt(7)
	v_mfma_i32_16x16x64_i8 v[158:161], v[106:109], v[164:167], v[158:161]
	v_mfma_i32_16x16x64_i8 v[154:157], v[114:117], v[164:167], v[154:157]
	s_waitcnt lgkmcnt(5)
	v_mfma_i32_16x16x64_i8 v[134:137], v[106:109], v[184:187], v[134:137]
	v_mfma_i32_16x16x64_i8 v[122:125], v[114:117], v[184:187], v[122:125]
	s_waitcnt lgkmcnt(3)
	v_mfma_i32_16x16x64_i8 v[94:97], v[106:109], v[192:195], v[94:97]
	v_mfma_i32_16x16x64_i8 v[90:93], v[114:117], v[192:195], v[90:93]
	s_waitcnt lgkmcnt(1)
	v_mfma_i32_16x16x64_i8 v[78:81], v[106:109], v[212:215], v[78:81]
	v_mfma_i32_16x16x64_i8 v[74:77], v[114:117], v[212:215], v[74:77]
	v_mfma_i32_16x16x64_i8 v[158:161], v[110:113], v[168:171], v[158:161]
	v_mfma_i32_16x16x64_i8 v[154:157], v[118:121], v[168:171], v[154:157]
	v_mfma_i32_16x16x64_i8 v[134:137], v[110:113], v[188:191], v[134:137]
	v_mfma_i32_16x16x64_i8 v[122:125], v[118:121], v[188:191], v[122:125]
	v_mfma_i32_16x16x64_i8 v[94:97], v[110:113], v[208:211], v[94:97]
	v_mfma_i32_16x16x64_i8 v[90:93], v[118:121], v[208:211], v[90:93]
	s_waitcnt lgkmcnt(0)
	v_mfma_i32_16x16x64_i8 v[78:81], v[110:113], v[216:219], v[78:81]
	v_mfma_i32_16x16x64_i8 v[74:77], v[118:121], v[216:219], v[74:77]
	s_setprio 1
	s_setprio 0
	v_mfma_i32_16x16x64_i8 v[150:153], v[126:129], v[164:167], v[150:153]
	v_mfma_i32_16x16x64_i8 v[146:149], v[138:141], v[164:167], v[146:149]
	v_mfma_i32_16x16x64_i8 v[102:105], v[126:129], v[184:187], v[102:105]
	v_mfma_i32_16x16x64_i8 v[98:101], v[138:141], v[184:187], v[98:101]
	v_mfma_i32_16x16x64_i8 v[86:89], v[126:129], v[192:195], v[86:89]
	v_mfma_i32_16x16x64_i8 v[82:85], v[138:141], v[192:195], v[82:85]
	v_mfma_i32_16x16x64_i8 v[70:73], v[126:129], v[212:215], v[70:73]
	v_mfma_i32_16x16x64_i8 v[66:69], v[138:141], v[212:215], v[66:69]
	v_mfma_i32_16x16x64_i8 v[150:153], v[130:133], v[168:171], v[150:153]
	v_mfma_i32_16x16x64_i8 v[146:149], v[142:145], v[168:171], v[146:149]
	v_mfma_i32_16x16x64_i8 v[102:105], v[130:133], v[188:191], v[102:105]
	v_mfma_i32_16x16x64_i8 v[98:101], v[142:145], v[188:191], v[98:101]
	v_mfma_i32_16x16x64_i8 v[86:89], v[130:133], v[208:211], v[86:89]
	v_mfma_i32_16x16x64_i8 v[82:85], v[142:145], v[208:211], v[82:85]
	v_mfma_i32_16x16x64_i8 v[70:73], v[130:133], v[216:219], v[70:73]
	v_mfma_i32_16x16x64_i8 v[66:69], v[142:145], v[216:219], v[66:69]
	s_setprio 1
	s_barrier
	s_mov_b32 s59, s85
	ds_read_b128 v[164:167], v178 offset:16384
	ds_read_b128 v[168:171], v178 offset:17408
	ds_read_b128 v[184:187], v178 offset:18432
	ds_read_b128 v[188:191], v178 offset:19456
	ds_read_b128 v[192:195], v178 offset:20480
	ds_read_b128 v[208:211], v178 offset:21504
	ds_read_b128 v[212:215], v178 offset:22528
	ds_read_b128 v[216:219], v178 offset:23552
	s_add_i32 m0, s59, 0x10000
	s_mov_b32 s59, s85
	buffer_load_dwordx4 v173, s[64:67], s53 offen lds
	s_add_i32 m0, s59, 0x12000
	s_mov_b32 s60, s85
	buffer_load_dwordx4 v175, s[64:67], s53 offen lds
	s_add_i32 s59, s53, 0x4000
	s_add_i32 m0, s60, 0x14000
	s_mov_b32 s60, s85
	buffer_load_dwordx4 v173, s[64:67], s59 offen lds
	s_add_i32 m0, s60, 0x16000
	s_nop 0
	buffer_load_dwordx4 v175, s[64:67], s59 offen lds
	s_mov_b32 s59, s85
	s_mov_b32 m0, s59
	s_mov_b32 s59, s85
	buffer_load_dwordx4 v172, s[88:91], s58 offen lds
	s_add_i32 m0, s59, 0x2000
	s_nop 0
	buffer_load_dwordx4 v174, s[88:91], s58 offen lds
	s_cmp_lg_u32 s55, 0
	s_cbranch_scc1 .Lgr17
	s_waitcnt vmcnt(8)
.Lgr17:
	s_waitcnt vmcnt(24)
	s_waitcnt lgkmcnt(0)
	s_barrier
	s_setprio 0
	s_waitcnt lgkmcnt(7)
	v_mfma_i32_16x16x64_i8 v[62:65], v[106:109], v[164:167], v[62:65]
	v_mfma_i32_16x16x64_i8 v[58:61], v[114:117], v[164:167], v[58:61]
	s_waitcnt lgkmcnt(5)
	v_mfma_i32_16x16x64_i8 v[46:49], v[106:109], v[184:187], v[46:49]
	v_mfma_i32_16x16x64_i8 v[42:45], v[114:117], v[184:187], v[42:45]
	s_waitcnt lgkmcnt(3)
	v_mfma_i32_16x16x64_i8 v[30:33], v[106:109], v[192:195], v[30:33]
	v_mfma_i32_16x16x64_i8 v[26:29], v[114:117], v[192:195], v[26:29]
	s_waitcnt lgkmcnt(1)
	v_mfma_i32_16x16x64_i8 v[14:17], v[106:109], v[212:215], v[14:17]
	v_mfma_i32_16x16x64_i8 v[10:13], v[114:117], v[212:215], v[10:13]
	v_mfma_i32_16x16x64_i8 v[62:65], v[110:113], v[168:171], v[62:65]
	v_mfma_i32_16x16x64_i8 v[58:61], v[118:121], v[168:171], v[58:61]
	v_mfma_i32_16x16x64_i8 v[46:49], v[110:113], v[188:191], v[46:49]
	v_mfma_i32_16x16x64_i8 v[42:45], v[118:121], v[188:191], v[42:45]
	v_mfma_i32_16x16x64_i8 v[30:33], v[110:113], v[208:211], v[30:33]
	v_mfma_i32_16x16x64_i8 v[26:29], v[118:121], v[208:211], v[26:29]
	s_waitcnt lgkmcnt(0)
	v_mfma_i32_16x16x64_i8 v[14:17], v[110:113], v[216:219], v[14:17]
	v_mfma_i32_16x16x64_i8 v[10:13], v[118:121], v[216:219], v[10:13]
	s_setprio 1
	s_setprio 0
	v_mfma_i32_16x16x64_i8 v[54:57], v[126:129], v[164:167], v[54:57]
	v_mfma_i32_16x16x64_i8 v[50:53], v[138:141], v[164:167], v[50:53]
	v_mfma_i32_16x16x64_i8 v[38:41], v[126:129], v[184:187], v[38:41]
	v_mfma_i32_16x16x64_i8 v[34:37], v[138:141], v[184:187], v[34:37]
	v_mfma_i32_16x16x64_i8 v[22:25], v[126:129], v[192:195], v[22:25]
	v_mfma_i32_16x16x64_i8 v[18:21], v[138:141], v[192:195], v[18:21]
	v_mfma_i32_16x16x64_i8 v[6:9], v[126:129], v[212:215], v[6:9]
	v_mfma_i32_16x16x64_i8 v[2:5], v[138:141], v[212:215], v[2:5]
	v_mfma_i32_16x16x64_i8 v[54:57], v[130:133], v[168:171], v[54:57]
	v_mfma_i32_16x16x64_i8 v[50:53], v[142:145], v[168:171], v[50:53]
	v_mfma_i32_16x16x64_i8 v[38:41], v[130:133], v[188:191], v[38:41]
	v_mfma_i32_16x16x64_i8 v[34:37], v[142:145], v[188:191], v[34:37]
	v_mfma_i32_16x16x64_i8 v[22:25], v[130:133], v[208:211], v[22:25]
	v_mfma_i32_16x16x64_i8 v[18:21], v[142:145], v[208:211], v[18:21]
	v_mfma_i32_16x16x64_i8 v[6:9], v[130:133], v[216:219], v[6:9]
	v_mfma_i32_16x16x64_i8 v[2:5], v[142:145], v[216:219], v[2:5]
	s_setprio 1
	s_barrier
	v_add_u32_e32 v118, 0x18000, v179
	v_add_u32_e32 v142, 0x1c000, v179
	ds_read_b128 v[106:109], v118
	ds_read_b128 v[110:113], v118 offset:1024
	ds_read_b128 v[114:117], v118 offset:2048
	ds_read_b128 v[118:121], v118 offset:3072
	ds_read_b128 v[126:129], v142
	ds_read_b128 v[130:133], v142 offset:1024
	ds_read_b128 v[138:141], v142 offset:2048
	ds_read_b128 v[142:145], v142 offset:3072
	s_mov_b32 s59, s85
	ds_read_b128 v[164:167], v178 offset:32768
	ds_read_b128 v[168:171], v178 offset:33792
	ds_read_b128 v[184:187], v178 offset:34816
	ds_read_b128 v[188:191], v178 offset:35840
	ds_read_b128 v[192:195], v178 offset:36864
	ds_read_b128 v[208:211], v178 offset:37888
	ds_read_b128 v[212:215], v178 offset:38912
	ds_read_b128 v[216:219], v178 offset:39936
	s_add_i32 s58, s58, 0x20000
	s_add_i32 m0, s59, 0x4000
	s_mov_b32 s59, s85
	buffer_load_dwordx4 v172, s[88:91], s58 offen lds
	s_add_i32 m0, s59, 0x6000
	s_nop 0
	buffer_load_dwordx4 v174, s[88:91], s58 offen lds
	s_cmp_lg_u32 s55, 0
	s_cbranch_scc1 .Lgr18
	s_waitcnt vmcnt(8)
; #define PG8_STAGE(bufoff, RS, soff, voff) do { _Pragma("unroll") for (int _i = 0; _i < 2; ++_i) \
;         __builtin_amdgcn_raw_ptr_buffer_load_lds(RS, (PG8_LAS void*)(lds + (bufoff) + sgpr_opaque(ldsw) + _i * 8192), 16, (int)(voff)[_i], (int)(soff), 0, 0); } while (0)
; #define PG8_LDA(dst, b, h) do { _Pragma("unroll") for (int m = 0; m < 4; ++m) _Pragma("unroll") for (int k = 0; k < 2; ++k) dst[m][k] = *(const PG8_LAS f16x8*)(lds + PG8_SA(b, h) + aoff + m * 2048 + k * 1024); } while (0)
; #define PG8_LDB(dst, b, h) do { _Pragma("unroll") for (int n = 0; n < 2; ++n) _Pragma("unroll") for (int k = 0; k < 2; ++k) dst[n][k] = *(const PG8_LAS f16x8*)(lds + PG8_SB(b, h) + boff + n * 2048 + k * 1024); } while (0)
; #define PG8_WAIT_L(n) asm volatile("s_waitcnt lgkmcnt(" #n ")" ::: "memory")
; #define PG8_BAR __builtin_amdgcn_s_barrier()
; #define PG8_SCHED __builtin_amdgcn_sched_barrier(0)
; template <class Epi, class Sched, bool ALIGN_EPI = false, bool SP2 = false, bool I8 = false, bool ATILED = false>
; __device__ __forceinline__ void gemm_phase(PG8_LAS unsigned char* lds, const Gemm g, const Sched& S, const Epi& E, const int wid) {
;     ...
;             PG8_LDB(B0, 0, 0); PG8_LDB(B1, 0, 1); PG8_SCHED; PG8_LDA(At, 0, 0); PG8_STAGE(PG8_SA(1, 1), rsA, a1 + hstepA, voffA);
;             PG8_WAIT_VG; PG8_WAIT_L(0); PG8_BAR; PG8_MMA(0, 0, At, B0); PG8_MMA(0, 1, At, B1); PG8_BAR; PG8_SCHED;
;             PG8_LDA(At, 0, 1); PG8_STAGE(PG8_SB(0, 0), rsB, b2, voffB); PG8_STAGE(PG8_SB(0, 1), rsB, b2 + hstep, voffB); PG8_STAGE(PG8_SA(0, 0), rsA, a2, voffA);
;             PG8_WAIT_VG; PG8_WAIT_L(0); PG8_BAR; PG8_MMA(1, 0, At, B0); PG8_MMA(1, 1, At, B1); PG8_BAR; PG8_SCHED;
;             PG8_LDB(B0, 1, 0); PG8_LDB(B1, 1, 1); PG8_SCHED; PG8_LDA(At, 1, 0); PG8_STAGE(PG8_SA(0, 1), rsA, a2 + hstepA, voffA);
;             PG8_WAIT_VG; PG8_WAIT_L(0); PG8_BAR; PG8_MMA(0, 0, At, B0); PG8_MMA(0, 1, At, B1); PG8_BAR; PG8_SCHED;
;             PG8_LDA(At, 1, 1); PG8_STAGE(PG8_SB(1, 0), rsB, b3, voffB); PG8_STAGE(PG8_SB(1, 1), rsB, b3 + hstep, voffB); PG8_STAGE(PG8_SA(1, 0), rsA, a3, voffA);
;             PG8_WAIT_VG; PG8_WAIT_L(0); PG8_BAR; PG8_MMA(1, 0, At, B0); PG8_MMA(1, 1, At, B1); PG8_BAR; PG8_SCHED;
.Lgr18:
	s_waitcnt vmcnt(24)
	s_waitcnt lgkmcnt(0)
	s_barrier
	s_setprio 0
	s_waitcnt lgkmcnt(7)
	v_mfma_i32_16x16x64_i8 v[158:161], v[106:109], v[164:167], v[158:161]
	v_mfma_i32_16x16x64_i8 v[154:157], v[114:117], v[164:167], v[154:157]
	s_waitcnt lgkmcnt(5)
	v_mfma_i32_16x16x64_i8 v[134:137], v[106:109], v[184:187], v[134:137]
	v_mfma_i32_16x16x64_i8 v[122:125], v[114:117], v[184:187], v[122:125]
	s_waitcnt lgkmcnt(3)
	v_mfma_i32_16x16x64_i8 v[94:97], v[106:109], v[192:195], v[94:97]
	v_mfma_i32_16x16x64_i8 v[90:93], v[114:117], v[192:195], v[90:93]
	s_waitcnt lgkmcnt(1)
	v_mfma_i32_16x16x64_i8 v[78:81], v[106:109], v[212:215], v[78:81]
	v_mfma_i32_16x16x64_i8 v[74:77], v[114:117], v[212:215], v[74:77]
	v_mfma_i32_16x16x64_i8 v[158:161], v[110:113], v[168:171], v[158:161]
	v_mfma_i32_16x16x64_i8 v[154:157], v[118:121], v[168:171], v[154:157]
	v_mfma_i32_16x16x64_i8 v[134:137], v[110:113], v[188:191], v[134:137]
	v_mfma_i32_16x16x64_i8 v[122:125], v[118:121], v[188:191], v[122:125]
	v_mfma_i32_16x16x64_i8 v[94:97], v[110:113], v[208:211], v[94:97]
	v_mfma_i32_16x16x64_i8 v[90:93], v[118:121], v[208:211], v[90:93]
	s_waitcnt lgkmcnt(0)
	v_mfma_i32_16x16x64_i8 v[78:81], v[110:113], v[216:219], v[78:81]
	v_mfma_i32_16x16x64_i8 v[74:77], v[118:121], v[216:219], v[74:77]
	s_setprio 1
	s_setprio 0
	v_mfma_i32_16x16x64_i8 v[150:153], v[126:129], v[164:167], v[150:153]
	v_mfma_i32_16x16x64_i8 v[146:149], v[138:141], v[164:167], v[146:149]
	v_mfma_i32_16x16x64_i8 v[102:105], v[126:129], v[184:187], v[102:105]
	v_mfma_i32_16x16x64_i8 v[98:101], v[138:141], v[184:187], v[98:101]
	v_mfma_i32_16x16x64_i8 v[86:89], v[126:129], v[192:195], v[86:89]
	v_mfma_i32_16x16x64_i8 v[82:85], v[138:141], v[192:195], v[82:85]
	v_mfma_i32_16x16x64_i8 v[70:73], v[126:129], v[212:215], v[70:73]
	v_mfma_i32_16x16x64_i8 v[66:69], v[138:141], v[212:215], v[66:69]
	v_mfma_i32_16x16x64_i8 v[150:153], v[130:133], v[168:171], v[150:153]
	v_mfma_i32_16x16x64_i8 v[146:149], v[142:145], v[168:171], v[146:149]
	v_mfma_i32_16x16x64_i8 v[102:105], v[130:133], v[188:191], v[102:105]
	v_mfma_i32_16x16x64_i8 v[98:101], v[142:145], v[188:191], v[98:101]
	v_mfma_i32_16x16x64_i8 v[86:89], v[130:133], v[208:211], v[86:89]
	v_mfma_i32_16x16x64_i8 v[82:85], v[142:145], v[208:211], v[82:85]
	v_mfma_i32_16x16x64_i8 v[70:73], v[130:133], v[216:219], v[70:73]
	v_mfma_i32_16x16x64_i8 v[66:69], v[142:145], v[216:219], v[66:69]
	s_setprio 1
	s_barrier
	s_mov_b32 s58, s85
	ds_read_b128 v[164:167], v178 offset:49152
	ds_read_b128 v[168:171], v178 offset:50176
	ds_read_b128 v[184:187], v178 offset:51200
	ds_read_b128 v[188:191], v178 offset:52224
	ds_read_b128 v[192:195], v178 offset:53248
	ds_read_b128 v[208:211], v178 offset:54272
	ds_read_b128 v[212:215], v178 offset:55296
	ds_read_b128 v[216:219], v178 offset:56320
	s_add_i32 m0, s58, 0x18000
	s_mov_b32 s58, s85
	buffer_load_dwordx4 v173, s[64:67], s54 offen lds
	s_add_i32 m0, s58, 0x1a000
	s_add_i32 s53, s53, 0xc000
	buffer_load_dwordx4 v175, s[64:67], s54 offen lds
	s_mov_b32 s54, s85
	s_add_i32 m0, s54, 0x1c000
	s_mov_b32 s54, s85
	buffer_load_dwordx4 v173, s[64:67], s53 offen lds
	s_add_i32 m0, s54, 0x1e000
	s_nop 0
	buffer_load_dwordx4 v175, s[64:67], s53 offen lds
	s_mov_b32 s53, s85
	s_add_i32 m0, s53, 0x8000
	s_mov_b32 s53, s85
	buffer_load_dwordx4 v172, s[88:91], s52 offen lds
	s_add_i32 m0, s53, 0xa000
	s_nop 0
	buffer_load_dwordx4 v174, s[88:91], s52 offen lds
	s_cmp_lg_u32 s55, 0
	s_cbranch_scc1 .Lgr19
	s_waitcnt vmcnt(8)
.Lgr19:
	s_waitcnt vmcnt(24)
	s_waitcnt lgkmcnt(0)
	s_barrier
	s_setprio 0
	s_waitcnt lgkmcnt(7)
	v_mfma_i32_16x16x64_i8 v[62:65], v[106:109], v[164:167], v[62:65]
	v_mfma_i32_16x16x64_i8 v[58:61], v[114:117], v[164:167], v[58:61]
	s_waitcnt lgkmcnt(5)
	v_mfma_i32_16x16x64_i8 v[46:49], v[106:109], v[184:187], v[46:49]
	v_mfma_i32_16x16x64_i8 v[42:45], v[114:117], v[184:187], v[42:45]
	s_waitcnt lgkmcnt(3)
	v_mfma_i32_16x16x64_i8 v[30:33], v[106:109], v[192:195], v[30:33]
	v_mfma_i32_16x16x64_i8 v[26:29], v[114:117], v[192:195], v[26:29]
	s_waitcnt lgkmcnt(1)
	v_mfma_i32_16x16x64_i8 v[14:17], v[106:109], v[212:215], v[14:17]
	v_mfma_i32_16x16x64_i8 v[10:13], v[114:117], v[212:215], v[10:13]
	v_mfma_i32_16x16x64_i8 v[62:65], v[110:113], v[168:171], v[62:65]
	v_mfma_i32_16x16x64_i8 v[58:61], v[118:121], v[168:171], v[58:61]
	v_mfma_i32_16x16x64_i8 v[46:49], v[110:113], v[188:191], v[46:49]
	v_mfma_i32_16x16x64_i8 v[42:45], v[118:121], v[188:191], v[42:45]
	v_mfma_i32_16x16x64_i8 v[30:33], v[110:113], v[208:211], v[30:33]
	v_mfma_i32_16x16x64_i8 v[26:29], v[118:121], v[208:211], v[26:29]
	s_waitcnt lgkmcnt(0)
	v_mfma_i32_16x16x64_i8 v[14:17], v[110:113], v[216:219], v[14:17]
	v_mfma_i32_16x16x64_i8 v[10:13], v[118:121], v[216:219], v[10:13]
	s_setprio 1
	s_setprio 0
	v_mfma_i32_16x16x64_i8 v[54:57], v[126:129], v[164:167], v[54:57]
	v_mfma_i32_16x16x64_i8 v[50:53], v[138:141], v[164:167], v[50:53]
	v_mfma_i32_16x16x64_i8 v[38:41], v[126:129], v[184:187], v[38:41]
	v_mfma_i32_16x16x64_i8 v[34:37], v[138:141], v[184:187], v[34:37]
	v_mfma_i32_16x16x64_i8 v[22:25], v[126:129], v[192:195], v[22:25]
	v_mfma_i32_16x16x64_i8 v[18:21], v[138:141], v[192:195], v[18:21]
	v_mfma_i32_16x16x64_i8 v[6:9], v[126:129], v[212:215], v[6:9]
	v_mfma_i32_16x16x64_i8 v[2:5], v[138:141], v[212:215], v[2:5]
	v_mfma_i32_16x16x64_i8 v[54:57], v[130:133], v[168:171], v[54:57]
	v_mfma_i32_16x16x64_i8 v[50:53], v[142:145], v[168:171], v[50:53]
	v_mfma_i32_16x16x64_i8 v[38:41], v[130:133], v[188:191], v[38:41]
	v_mfma_i32_16x16x64_i8 v[34:37], v[142:145], v[188:191], v[34:37]
	v_mfma_i32_16x16x64_i8 v[22:25], v[130:133], v[208:211], v[22:25]
	v_mfma_i32_16x16x64_i8 v[18:21], v[142:145], v[208:211], v[18:21]
	v_mfma_i32_16x16x64_i8 v[6:9], v[130:133], v[216:219], v[6:9]
	v_mfma_i32_16x16x64_i8 v[2:5], v[142:145], v[216:219], v[2:5]
	s_setprio 1
	s_barrier
	s_add_i32 s51, s51, 2
	s_addk_i32 s49, 0x100
	s_add_i32 s50, s50, 0x10000
	s_cmp_gt_u32 s51, 5
	s_cbranch_scc0 .LBB0_1611
	s_and_b64 vcc, exec, s[56:57]
	s_cbranch_vccz .LBB0_1614
	s_barrier

; #define PG8_STAGE(bufoff, RS, soff, voff) do { _Pragma("unroll") for (int _i = 0; _i < 2; ++_i) \
;         __builtin_amdgcn_raw_ptr_buffer_load_lds(RS, (PG8_LAS void*)(lds + (bufoff) + sgpr_opaque(ldsw) + _i * 8192), 16, (int)(voff)[_i], (int)(soff), 0, 0); } while (0)
; #define PG8_LDA(dst, b, h) do { _Pragma("unroll") for (int m = 0; m < 4; ++m) _Pragma("unroll") for (int k = 0; k < 2; ++k) dst[m][k] = *(const PG8_LAS f16x8*)(lds + PG8_SA(b, h) + aoff + m * 2048 + k * 1024); } while (0)
; #define PG8_LDB(dst, b, h) do { _Pragma("unroll") for (int n = 0; n < 2; ++n) _Pragma("unroll") for (int k = 0; k < 2; ++k) dst[n][k] = *(const PG8_LAS f16x8*)(lds + PG8_SB(b, h) + boff + n * 2048 + k * 1024); } while (0)
; #define PG8_WAIT_L(n) asm volatile("s_waitcnt lgkmcnt(" #n ")" ::: "memory")
; #define PG8_BAR __builtin_amdgcn_s_barrier()
; #define PG8_SCHED __builtin_amdgcn_sched_barrier(0)
; template <class Epi, class Sched, bool ALIGN_EPI = false, bool SP2 = false, bool I8 = false, bool ATILED = false>
; __device__ __forceinline__ void gemm_phase(PG8_LAS unsigned char* lds, const Gemm g, const Sched& S, const Epi& E, const int wid) {
;     ...
;             PG8_LDB(B0, 0, 0); PG8_LDB(B1, 0, 1); PG8_SCHED; PG8_LDA(At, 0, 0); PG8_STAGE(PG8_SA(1, 1), rsA, a1 + hstepA, voffA);
;             PG8_WAIT_VG; PG8_WAIT_L(0); PG8_BAR; PG8_MMA(0, 0, At, B0); PG8_MMA(0, 1, At, B1); PG8_BAR; PG8_SCHED;
;             PG8_LDA(At, 0, 1); PG8_STAGE(PG8_SB(0, 0), rsB, b2, voffB); PG8_STAGE(PG8_SB(0, 1), rsB, b2 + hstep, voffB); PG8_STAGE(PG8_SA(0, 0), rsA, a2, voffA);
;             PG8_WAIT_VG; PG8_WAIT_L(0); PG8_BAR; PG8_MMA(1, 0, At, B0); PG8_MMA(1, 1, At, B1); PG8_BAR; PG8_SCHED;
;             PG8_LDB(B0, 1, 0); PG8_LDB(B1, 1, 1); PG8_SCHED; PG8_LDA(At, 1, 0); PG8_STAGE(PG8_SA(0, 1), rsA, a2 + hstepA, voffA);
;             PG8_WAIT_VG; PG8_WAIT_L(0); PG8_BAR; PG8_MMA(0, 0, At, B0); PG8_MMA(0, 1, At, B1); PG8_BAR; PG8_SCHED;
;             PG8_LDA(At, 1, 1); PG8_STAGE(PG8_SB(1, 0), rsB, b3, voffB); PG8_STAGE(PG8_SB(1, 1), rsB, b3 + hstep, voffB); PG8_STAGE(PG8_SA(1, 0), rsA, a3, voffA);
;             PG8_WAIT_VG; PG8_WAIT_L(0); PG8_BAR; PG8_MMA(1, 0, At, B0); PG8_MMA(1, 1, At, B1); PG8_BAR; PG8_SCHED;
.Lgr20:
	s_waitcnt vmcnt(40)
	s_waitcnt lgkmcnt(0)
	s_barrier
	s_setprio 0
	s_waitcnt lgkmcnt(7)
	v_mfma_f32_16x16x32_f16 v[142:145], v[106:109], v[162:165], v[142:145]
	v_mfma_f32_16x16x32_f16 v[138:141], v[114:117], v[162:165], v[138:141]
	s_waitcnt lgkmcnt(5)
	v_mfma_f32_16x16x32_f16 v[126:129], v[106:109], v[170:173], v[126:129]
	v_mfma_f32_16x16x32_f16 v[118:121], v[114:117], v[170:173], v[118:121]
	s_waitcnt lgkmcnt(3)
	v_mfma_f32_16x16x32_f16 v[98:101], v[106:109], v[178:181], v[98:101]
	v_mfma_f32_16x16x32_f16 v[90:93], v[114:117], v[178:181], v[90:93]
	s_waitcnt lgkmcnt(1)
	v_mfma_f32_16x16x32_f16 v[82:85], v[106:109], v[194:197], v[82:85]
	v_mfma_f32_16x16x32_f16 v[74:77], v[114:117], v[194:197], v[74:77]
	v_mfma_f32_16x16x32_f16 v[142:145], v[110:113], v[166:169], v[142:145]
	v_mfma_f32_16x16x32_f16 v[138:141], v[122:125], v[166:169], v[138:141]
	v_mfma_f32_16x16x32_f16 v[126:129], v[110:113], v[174:177], v[126:129]
	v_mfma_f32_16x16x32_f16 v[118:121], v[122:125], v[174:177], v[118:121]
	v_mfma_f32_16x16x32_f16 v[98:101], v[110:113], v[182:185], v[98:101]
	v_mfma_f32_16x16x32_f16 v[90:93], v[122:125], v[182:185], v[90:93]
	s_waitcnt lgkmcnt(0)
	v_mfma_f32_16x16x32_f16 v[82:85], v[110:113], v[208:211], v[82:85]
	v_mfma_f32_16x16x32_f16 v[74:77], v[122:125], v[208:211], v[74:77]
	s_setprio 1
	s_setprio 0
	v_mfma_f32_16x16x32_f16 v[134:137], v[146:149], v[162:165], v[134:137]
	v_mfma_f32_16x16x32_f16 v[130:133], v[154:157], v[162:165], v[130:133]
	v_mfma_f32_16x16x32_f16 v[102:105], v[146:149], v[170:173], v[102:105]
	v_mfma_f32_16x16x32_f16 v[94:97], v[154:157], v[170:173], v[94:97]
	v_mfma_f32_16x16x32_f16 v[86:89], v[146:149], v[178:181], v[86:89]
	v_mfma_f32_16x16x32_f16 v[78:81], v[154:157], v[178:181], v[78:81]
	v_mfma_f32_16x16x32_f16 v[70:73], v[146:149], v[194:197], v[70:73]
	v_mfma_f32_16x16x32_f16 v[66:69], v[154:157], v[194:197], v[66:69]
	v_mfma_f32_16x16x32_f16 v[134:137], v[150:153], v[166:169], v[134:137]
	v_mfma_f32_16x16x32_f16 v[130:133], v[158:161], v[166:169], v[130:133]
	v_mfma_f32_16x16x32_f16 v[102:105], v[150:153], v[174:177], v[102:105]
	v_mfma_f32_16x16x32_f16 v[94:97], v[158:161], v[174:177], v[94:97]
	v_mfma_f32_16x16x32_f16 v[86:89], v[150:153], v[182:185], v[86:89]
	v_mfma_f32_16x16x32_f16 v[78:81], v[158:161], v[182:185], v[78:81]
	v_mfma_f32_16x16x32_f16 v[70:73], v[150:153], v[208:211], v[70:73]
	v_mfma_f32_16x16x32_f16 v[66:69], v[158:161], v[208:211], v[66:69]
	s_setprio 1
	s_barrier
	s_mov_b32 s38, s85
	ds_read_b128 v[162:165], v190 offset:16384
	ds_read_b128 v[166:169], v190 offset:17408
	ds_read_b128 v[170:173], v190 offset:18432
	ds_read_b128 v[174:177], v190 offset:19456
	ds_read_b128 v[178:181], v190 offset:20480
	ds_read_b128 v[182:185], v190 offset:21504
	ds_read_b128 v[194:197], v190 offset:22528
	ds_read_b128 v[208:211], v190 offset:23552
	s_add_i32 m0, s38, 0x10000
	s_mov_b32 s38, s66
	s_mov_b32 s39, s67
	s_mov_b32 s62, s85
	buffer_load_dwordx4 v186, s[36:39], s58 offen lds
	s_add_i32 m0, s62, 0x12000
	s_mov_b32 s63, s85
	buffer_load_dwordx4 v188, s[36:39], s58 offen lds
	s_add_i32 s62, s58, 0x100000
	s_add_i32 m0, s63, 0x14000
	s_mov_b32 s63, s85
	buffer_load_dwordx4 v186, s[36:39], s62 offen lds
	s_add_i32 m0, s63, 0x16000
	s_nop 0
	buffer_load_dwordx4 v188, s[36:39], s62 offen lds
	s_mov_b32 s62, s85
	s_mov_b32 m0, s62
	s_mov_b32 s62, s85
	buffer_load_dwordx4 v0, s[64:67], s61 offen lds
	s_add_i32 m0, s62, 0x2000
	s_nop 0
	buffer_load_dwordx4 v187, s[64:67], s61 offen lds
	s_cmp_lg_u32 s60, 0
	s_cbranch_scc1 .Lgr21
	s_waitcnt vmcnt(8)
.Lgr21:
	s_waitcnt vmcnt(40)
	s_waitcnt lgkmcnt(0)
	s_barrier
	s_setprio 0
	s_waitcnt lgkmcnt(7)
	v_mfma_f32_16x16x32_f16 v[62:65], v[106:109], v[162:165], v[62:65]
	v_mfma_f32_16x16x32_f16 v[58:61], v[114:117], v[162:165], v[58:61]
	s_waitcnt lgkmcnt(5)
	v_mfma_f32_16x16x32_f16 v[50:53], v[106:109], v[170:173], v[50:53]
	v_mfma_f32_16x16x32_f16 v[42:45], v[114:117], v[170:173], v[42:45]
	s_waitcnt lgkmcnt(3)
	v_mfma_f32_16x16x32_f16 v[34:37], v[106:109], v[178:181], v[34:37]
	v_mfma_f32_16x16x32_f16 v[26:29], v[114:117], v[178:181], v[26:29]
	s_waitcnt lgkmcnt(1)
	v_mfma_f32_16x16x32_f16 v[18:21], v[106:109], v[194:197], v[18:21]
	v_mfma_f32_16x16x32_f16 v[10:13], v[114:117], v[194:197], v[10:13]
	v_mfma_f32_16x16x32_f16 v[62:65], v[110:113], v[166:169], v[62:65]
	v_mfma_f32_16x16x32_f16 v[58:61], v[122:125], v[166:169], v[58:61]
	v_mfma_f32_16x16x32_f16 v[50:53], v[110:113], v[174:177], v[50:53]
	v_mfma_f32_16x16x32_f16 v[42:45], v[122:125], v[174:177], v[42:45]
	v_mfma_f32_16x16x32_f16 v[34:37], v[110:113], v[182:185], v[34:37]
	v_mfma_f32_16x16x32_f16 v[26:29], v[122:125], v[182:185], v[26:29]
	s_waitcnt lgkmcnt(0)
	v_mfma_f32_16x16x32_f16 v[18:21], v[110:113], v[208:211], v[18:21]
	v_mfma_f32_16x16x32_f16 v[10:13], v[122:125], v[208:211], v[10:13]
	s_setprio 1
	s_setprio 0
	v_mfma_f32_16x16x32_f16 v[54:57], v[146:149], v[162:165], v[54:57]
	v_mfma_f32_16x16x32_f16 v[46:49], v[154:157], v[162:165], v[46:49]
	v_mfma_f32_16x16x32_f16 v[38:41], v[146:149], v[170:173], v[38:41]
	v_mfma_f32_16x16x32_f16 v[30:33], v[154:157], v[170:173], v[30:33]
	v_mfma_f32_16x16x32_f16 v[22:25], v[146:149], v[178:181], v[22:25]
	v_mfma_f32_16x16x32_f16 v[14:17], v[154:157], v[178:181], v[14:17]
	v_mfma_f32_16x16x32_f16 v[6:9], v[146:149], v[194:197], v[6:9]
	v_mfma_f32_16x16x32_f16 v[2:5], v[154:157], v[194:197], v[2:5]
	v_mfma_f32_16x16x32_f16 v[54:57], v[150:153], v[166:169], v[54:57]
	v_mfma_f32_16x16x32_f16 v[46:49], v[158:161], v[166:169], v[46:49]
	v_mfma_f32_16x16x32_f16 v[38:41], v[150:153], v[174:177], v[38:41]
	v_mfma_f32_16x16x32_f16 v[30:33], v[158:161], v[174:177], v[30:33]
	v_mfma_f32_16x16x32_f16 v[22:25], v[150:153], v[182:185], v[22:25]
	v_mfma_f32_16x16x32_f16 v[14:17], v[158:161], v[182:185], v[14:17]
	v_mfma_f32_16x16x32_f16 v[6:9], v[150:153], v[208:211], v[6:9]
	v_mfma_f32_16x16x32_f16 v[2:5], v[158:161], v[208:211], v[2:5]
	s_setprio 1
	s_barrier
	v_add_u32_e32 v122, 0x18000, v191
	v_add_u32_e32 v158, 0x1c000, v191
	ds_read_b128 v[106:109], v122
	ds_read_b128 v[110:113], v122 offset:1024
	ds_read_b128 v[114:117], v122 offset:2048
	ds_read_b128 v[122:125], v122 offset:3072
	ds_read_b128 v[146:149], v158
	ds_read_b128 v[150:153], v158 offset:1024
	ds_read_b128 v[154:157], v158 offset:2048
	ds_read_b128 v[158:161], v158 offset:3072
	s_mov_b32 s62, s85
	ds_read_b128 v[162:165], v190 offset:32768
	ds_read_b128 v[166:169], v190 offset:33792
	ds_read_b128 v[170:173], v190 offset:34816
	ds_read_b128 v[174:177], v190 offset:35840
	ds_read_b128 v[178:181], v190 offset:36864
	ds_read_b128 v[182:185], v190 offset:37888
	ds_read_b128 v[194:197], v190 offset:38912
	ds_read_b128 v[208:211], v190 offset:39936
	s_bitset1_b32 s61, 14
	s_add_i32 m0, s62, 0x4000
	s_mov_b32 s62, s85
	buffer_load_dwordx4 v0, s[64:67], s61 offen lds
	s_add_i32 m0, s62, 0x6000
	s_nop 0
	buffer_load_dwordx4 v187, s[64:67], s61 offen lds
	s_cmp_lg_u32 s60, 0
	s_cbranch_scc1 .Lgr22
	s_waitcnt vmcnt(8)
; #define PG8_STAGE(bufoff, RS, soff, voff) do { _Pragma("unroll") for (int _i = 0; _i < 2; ++_i) \
;         __builtin_amdgcn_raw_ptr_buffer_load_lds(RS, (PG8_LAS void*)(lds + (bufoff) + sgpr_opaque(ldsw) + _i * 8192), 16, (int)(voff)[_i], (int)(soff), 0, 0); } while (0)
; #define PG8_LDA(dst, b, h) do { _Pragma("unroll") for (int m = 0; m < 4; ++m) _Pragma("unroll") for (int k = 0; k < 2; ++k) dst[m][k] = *(const PG8_LAS f16x8*)(lds + PG8_SA(b, h) + aoff + m * 2048 + k * 1024); } while (0)
; #define PG8_LDB(dst, b, h) do { _Pragma("unroll") for (int n = 0; n < 2; ++n) _Pragma("unroll") for (int k = 0; k < 2; ++k) dst[n][k] = *(const PG8_LAS f16x8*)(lds + PG8_SB(b, h) + boff + n * 2048 + k * 1024); } while (0)
; #define PG8_WAIT_L(n) asm volatile("s_waitcnt lgkmcnt(" #n ")" ::: "memory")
; #define PG8_BAR __builtin_amdgcn_s_barrier()
; #define PG8_SCHED __builtin_amdgcn_sched_barrier(0)
; template <class Epi, class Sched, bool ALIGN_EPI = false, bool SP2 = false, bool I8 = false, bool ATILED = false>
; __device__ __forceinline__ void gemm_phase(PG8_LAS unsigned char* lds, const Gemm g, const Sched& S, const Epi& E, const int wid) {
;     ...
;             PG8_LDB(B0, 0, 0); PG8_LDB(B1, 0, 1); PG8_SCHED; PG8_LDA(At, 0, 0); PG8_STAGE(PG8_SA(1, 1), rsA, a1 + hstepA, voffA);
;             PG8_WAIT_VG; PG8_WAIT_L(0); PG8_BAR; PG8_MMA(0, 0, At, B0); PG8_MMA(0, 1, At, B1); PG8_BAR; PG8_SCHED;
;             PG8_LDA(At, 0, 1); PG8_STAGE(PG8_SB(0, 0), rsB, b2, voffB); PG8_STAGE(PG8_SB(0, 1), rsB, b2 + hstep, voffB); PG8_STAGE(PG8_SA(0, 0), rsA, a2, voffA);
;             PG8_WAIT_VG; PG8_WAIT_L(0); PG8_BAR; PG8_MMA(1, 0, At, B0); PG8_MMA(1, 1, At, B1); PG8_BAR; PG8_SCHED;
;             PG8_LDB(B0, 1, 0); PG8_LDB(B1, 1, 1); PG8_SCHED; PG8_LDA(At, 1, 0); PG8_STAGE(PG8_SA(0, 1), rsA, a2 + hstepA, voffA);
;             PG8_WAIT_VG; PG8_WAIT_L(0); PG8_BAR; PG8_MMA(0, 0, At, B0); PG8_MMA(0, 1, At, B1); PG8_BAR; PG8_SCHED;
;             PG8_LDA(At, 1, 1); PG8_STAGE(PG8_SB(1, 0), rsB, b3, voffB); PG8_STAGE(PG8_SB(1, 1), rsB, b3 + hstep, voffB); PG8_STAGE(PG8_SA(1, 0), rsA, a3, voffA);
;             PG8_WAIT_VG; PG8_WAIT_L(0); PG8_BAR; PG8_MMA(1, 0, At, B0); PG8_MMA(1, 1, At, B1); PG8_BAR; PG8_SCHED;
.Lgr22:
	s_waitcnt vmcnt(40)
	s_waitcnt lgkmcnt(0)
	s_barrier
	s_setprio 0
	s_waitcnt lgkmcnt(7)
	v_mfma_f32_16x16x32_f16 v[142:145], v[106:109], v[162:165], v[142:145]
	v_mfma_f32_16x16x32_f16 v[138:141], v[114:117], v[162:165], v[138:141]
	s_waitcnt lgkmcnt(5)
	v_mfma_f32_16x16x32_f16 v[126:129], v[106:109], v[170:173], v[126:129]
	v_mfma_f32_16x16x32_f16 v[118:121], v[114:117], v[170:173], v[118:121]
	s_waitcnt lgkmcnt(3)
	v_mfma_f32_16x16x32_f16 v[98:101], v[106:109], v[178:181], v[98:101]
	v_mfma_f32_16x16x32_f16 v[90:93], v[114:117], v[178:181], v[90:93]
	s_waitcnt lgkmcnt(1)
	v_mfma_f32_16x16x32_f16 v[82:85], v[106:109], v[194:197], v[82:85]
	v_mfma_f32_16x16x32_f16 v[74:77], v[114:117], v[194:197], v[74:77]
	v_mfma_f32_16x16x32_f16 v[142:145], v[110:113], v[166:169], v[142:145]
	v_mfma_f32_16x16x32_f16 v[138:141], v[122:125], v[166:169], v[138:141]
	v_mfma_f32_16x16x32_f16 v[126:129], v[110:113], v[174:177], v[126:129]
	v_mfma_f32_16x16x32_f16 v[118:121], v[122:125], v[174:177], v[118:121]
	v_mfma_f32_16x16x32_f16 v[98:101], v[110:113], v[182:185], v[98:101]
	v_mfma_f32_16x16x32_f16 v[90:93], v[122:125], v[182:185], v[90:93]
	s_waitcnt lgkmcnt(0)
	v_mfma_f32_16x16x32_f16 v[82:85], v[110:113], v[208:211], v[82:85]
	v_mfma_f32_16x16x32_f16 v[74:77], v[122:125], v[208:211], v[74:77]
	s_setprio 1
	s_setprio 0
	v_mfma_f32_16x16x32_f16 v[134:137], v[146:149], v[162:165], v[134:137]
	v_mfma_f32_16x16x32_f16 v[130:133], v[154:157], v[162:165], v[130:133]
	v_mfma_f32_16x16x32_f16 v[102:105], v[146:149], v[170:173], v[102:105]
	v_mfma_f32_16x16x32_f16 v[94:97], v[154:157], v[170:173], v[94:97]
	v_mfma_f32_16x16x32_f16 v[86:89], v[146:149], v[178:181], v[86:89]
	v_mfma_f32_16x16x32_f16 v[78:81], v[154:157], v[178:181], v[78:81]
	v_mfma_f32_16x16x32_f16 v[70:73], v[146:149], v[194:197], v[70:73]
	v_mfma_f32_16x16x32_f16 v[66:69], v[154:157], v[194:197], v[66:69]
	v_mfma_f32_16x16x32_f16 v[134:137], v[150:153], v[166:169], v[134:137]
	v_mfma_f32_16x16x32_f16 v[130:133], v[158:161], v[166:169], v[130:133]
	v_mfma_f32_16x16x32_f16 v[102:105], v[150:153], v[174:177], v[102:105]
	v_mfma_f32_16x16x32_f16 v[94:97], v[158:161], v[174:177], v[94:97]
	v_mfma_f32_16x16x32_f16 v[86:89], v[150:153], v[182:185], v[86:89]
	v_mfma_f32_16x16x32_f16 v[78:81], v[158:161], v[182:185], v[78:81]
	v_mfma_f32_16x16x32_f16 v[70:73], v[150:153], v[208:211], v[70:73]
	v_mfma_f32_16x16x32_f16 v[66:69], v[158:161], v[208:211], v[66:69]
	s_setprio 1
	s_barrier
	s_mov_b32 s61, s85
	ds_read_b128 v[162:165], v190 offset:49152
	ds_read_b128 v[166:169], v190 offset:50176
	ds_read_b128 v[170:173], v190 offset:51200
	ds_read_b128 v[174:177], v190 offset:52224
	ds_read_b128 v[178:181], v190 offset:53248
	ds_read_b128 v[182:185], v190 offset:54272
	ds_read_b128 v[194:197], v190 offset:55296
	ds_read_b128 v[208:211], v190 offset:56320
	s_add_i32 m0, s61, 0x18000
	s_mov_b32 s61, s85
	buffer_load_dwordx4 v186, s[36:39], s59 offen lds
	s_add_i32 m0, s61, 0x1a000
	s_add_i32 s58, s58, 0x100080
	buffer_load_dwordx4 v188, s[36:39], s59 offen lds
	s_mov_b32 s59, s85
	s_add_i32 m0, s59, 0x1c000
	s_mov_b32 s59, s85
	buffer_load_dwordx4 v186, s[36:39], s58 offen lds
	s_add_i32 m0, s59, 0x1e000
	s_nop 0
	buffer_load_dwordx4 v188, s[36:39], s58 offen lds
	s_mov_b32 s38, s85
	s_add_i32 m0, s38, 0x8000
	s_mov_b32 s38, s85
	buffer_load_dwordx4 v0, s[64:67], s55 offen lds
	s_add_i32 m0, s38, 0xa000
	s_nop 0
	buffer_load_dwordx4 v187, s[64:67], s55 offen lds
	s_cmp_lg_u32 s60, 0
	s_cbranch_scc1 .Lgr23
	s_waitcnt vmcnt(8)
.Lgr23:
	s_waitcnt vmcnt(40)
	s_waitcnt lgkmcnt(0)
	s_barrier
	s_setprio 0
	s_waitcnt lgkmcnt(7)
	v_mfma_f32_16x16x32_f16 v[62:65], v[106:109], v[162:165], v[62:65]
	v_mfma_f32_16x16x32_f16 v[58:61], v[114:117], v[162:165], v[58:61]
	s_waitcnt lgkmcnt(5)
	v_mfma_f32_16x16x32_f16 v[50:53], v[106:109], v[170:173], v[50:53]
	v_mfma_f32_16x16x32_f16 v[42:45], v[114:117], v[170:173], v[42:45]
	s_waitcnt lgkmcnt(3)
	v_mfma_f32_16x16x32_f16 v[34:37], v[106:109], v[178:181], v[34:37]
	v_mfma_f32_16x16x32_f16 v[26:29], v[114:117], v[178:181], v[26:29]
	s_waitcnt lgkmcnt(1)
	v_mfma_f32_16x16x32_f16 v[18:21], v[106:109], v[194:197], v[18:21]
	v_mfma_f32_16x16x32_f16 v[10:13], v[114:117], v[194:197], v[10:13]
	v_mfma_f32_16x16x32_f16 v[62:65], v[110:113], v[166:169], v[62:65]
	v_mfma_f32_16x16x32_f16 v[58:61], v[122:125], v[166:169], v[58:61]
	v_mfma_f32_16x16x32_f16 v[50:53], v[110:113], v[174:177], v[50:53]
	v_mfma_f32_16x16x32_f16 v[42:45], v[122:125], v[174:177], v[42:45]
	v_mfma_f32_16x16x32_f16 v[34:37], v[110:113], v[182:185], v[34:37]
	v_mfma_f32_16x16x32_f16 v[26:29], v[122:125], v[182:185], v[26:29]
	s_waitcnt lgkmcnt(0)
	v_mfma_f32_16x16x32_f16 v[18:21], v[110:113], v[208:211], v[18:21]
	v_mfma_f32_16x16x32_f16 v[10:13], v[122:125], v[208:211], v[10:13]
	s_setprio 1
	s_setprio 0
	v_mfma_f32_16x16x32_f16 v[54:57], v[146:149], v[162:165], v[54:57]
	v_mfma_f32_16x16x32_f16 v[46:49], v[154:157], v[162:165], v[46:49]
	v_mfma_f32_16x16x32_f16 v[38:41], v[146:149], v[170:173], v[38:41]
	v_mfma_f32_16x16x32_f16 v[30:33], v[154:157], v[170:173], v[30:33]
	v_mfma_f32_16x16x32_f16 v[22:25], v[146:149], v[178:181], v[22:25]
	v_mfma_f32_16x16x32_f16 v[14:17], v[154:157], v[178:181], v[14:17]
	v_mfma_f32_16x16x32_f16 v[6:9], v[146:149], v[194:197], v[6:9]
	v_mfma_f32_16x16x32_f16 v[2:5], v[154:157], v[194:197], v[2:5]
	v_mfma_f32_16x16x32_f16 v[54:57], v[150:153], v[166:169], v[54:57]
	v_mfma_f32_16x16x32_f16 v[46:49], v[158:161], v[166:169], v[46:49]
	v_mfma_f32_16x16x32_f16 v[38:41], v[150:153], v[174:177], v[38:41]
	v_mfma_f32_16x16x32_f16 v[30:33], v[158:161], v[174:177], v[30:33]
	v_mfma_f32_16x16x32_f16 v[22:25], v[150:153], v[182:185], v[22:25]
	v_mfma_f32_16x16x32_f16 v[14:17], v[158:161], v[182:185], v[14:17]
	v_mfma_f32_16x16x32_f16 v[6:9], v[150:153], v[208:211], v[6:9]
	v_mfma_f32_16x16x32_f16 v[2:5], v[158:161], v[208:211], v[2:5]
	s_setprio 1
	s_barrier
	s_addk_i32 s53, 0x100
	s_add_i32 s54, s54, 2
	s_add_i32 s52, s52, 0x10000
	s_cmp_gt_u32 s54, 61
	s_cbranch_scc0 .LBB0_1701
	s_and_b64 vcc, exec, s[56:57]
	s_cbranch_vccz .LBB0_1704
	s_barrier
